# speedup vs baseline: 1.0137x; 1.0031x over previous
_Z15qkv_proj_kernelPKDF16_S0_PKfS2_S2_PDF16_S3_S3_:
	s_lshr_b32 s4, s2, 2
	s_and_b32 s3, s2, 7
	s_and_b32 s22, s4, 8
	s_or_b32 s4, s22, s3
	v_readfirstlane_b32 s18, v0
	s_ashr_i32 s3, s2, 6
	s_lshl_b32 s21, s4, 8
	s_bfe_u32 s20, s2, 0x20003
	v_and_b32_e32 v1, 63, v0
	s_cmpk_lt_u32 s18, 0x200
	s_mulk_i32 s20, 0xc0
	s_cbranch_scc1 .LBB1_30
	s_setprio 2
	s_load_dwordx4 s[4:7], s[0:1], 0x0
	s_sub_i32 s10, 2, s3
	s_lshr_b32 s12, s18, 6
	s_add_i32 s12, s12, -8
	s_mul_i32 s13, s10, 0x600000
	s_mul_hi_i32 s14, s10, 0x600000
	s_mul_i32 s15, s10, 0x120000
	s_waitcnt lgkmcnt(0)
	s_add_u32 s4, s4, s13
	s_addc_u32 s5, s5, s14
	s_add_u32 s6, s6, s15
	s_addc_u32 s7, s7, 0
	v_lshrrev_b32_e32 v2, 2, v1
	v_lshrrev_b32_e32 v3, 4, v1
	v_xor_b32_e32 v3, v3, v1
	v_and_b32_e32 v3, 3, v3
	v_lshlrev_b32_e32 v3, 4, v3
	v_mul_u32_u24_e32 v2, 0x600, v2
	v_add_u32_e32 v2, v2, v3
	s_mul_i32 s16, s12, 7
	s_mul_i32 s27, s20, 0x600
	s_add_u32 s6, s6, s27
	s_addc_u32 s7, s7, 0
	s_add_i32 s27, s21, -192
	s_mul_i32 s27, s27, 0x600
	s_ashr_i32 s28, s27, 31
	s_add_u32 s4, s4, s27
	s_addc_u32 s5, s5, s28
	s_add_i32 s17, s16, 0
	s_cmp_ge_u32 s17, 12
	s_cselect_b32 s24, s4, s6
	s_cselect_b32 s25, s5, s7
	s_mul_i32 s17, s17, 0x6000
	s_add_u32 s30, s24, s17
	s_addc_u32 s31, s25, 0
	s_add_i32 s17, s16, 1
	s_cmp_ge_u32 s17, 12
	s_cselect_b32 s24, s4, s6
	s_cselect_b32 s25, s5, s7
	s_mul_i32 s17, s17, 0x6000
	s_add_u32 s32, s24, s17
	s_addc_u32 s33, s25, 0
	s_add_i32 s17, s16, 2
	s_cmp_ge_u32 s17, 12
	s_cselect_b32 s24, s4, s6
	s_cselect_b32 s25, s5, s7
	s_mul_i32 s17, s17, 0x6000
	s_add_u32 s34, s24, s17
	s_addc_u32 s35, s25, 0
	s_add_i32 s17, s16, 3
	s_cmp_ge_u32 s17, 12
	s_cselect_b32 s24, s4, s6
	s_cselect_b32 s25, s5, s7
	s_mul_i32 s17, s17, 0x6000
	s_add_u32 s36, s24, s17
	s_addc_u32 s37, s25, 0
	s_add_i32 s17, s16, 4
	s_cmp_ge_u32 s17, 12
	s_cselect_b32 s24, s4, s6
	s_cselect_b32 s25, s5, s7
	s_mul_i32 s17, s17, 0x6000
	s_add_u32 s38, s24, s17
	s_addc_u32 s39, s25, 0
	s_add_i32 s17, s16, 5
	s_cmp_ge_u32 s17, 12
	s_cselect_b32 s24, s4, s6
	s_cselect_b32 s25, s5, s7
	s_mul_i32 s17, s17, 0x6000
	s_add_u32 s40, s24, s17
	s_addc_u32 s41, s25, 0
	s_add_i32 s17, s16, 6
	s_cmp_ge_u32 s17, 12
	s_cselect_b32 s24, s4, s6
	s_cselect_b32 s25, s5, s7
	s_mul_i32 s17, s17, 0x6000
	s_add_u32 s42, s24, s17
	s_addc_u32 s43, s25, 0
	s_mul_i32 s26, s12, 0x1c00
	s_lshl_b32 s11, s10, 3
	s_add_i32 s11, s11, 0x10
	s_load_dwordx2 s[8:9], s[0:1], s11
	s_cmp_eq_u32 s10, 0
	s_cselect_b32 s29, 0x3e38aa3b, 1.0
	v_lshl_add_u32 v19, s12, 6, v1
	v_lshlrev_b32_e32 v21, 2, v19
	v_add_u32_e32 v21, 0x23800, v21
	v_min_u32_e32 v19, 0xbf, v19
	v_add_u32_e32 v19, s20, v19
	v_lshlrev_b32_e32 v19, 2, v19
	s_waitcnt lgkmcnt(0)
	global_load_dword v20, v19, s[8:9]
	s_add_i32 m0, s26, 2048
	s_nop 0
	global_load_lds_dwordx4 v2, s[30:31]
	s_add_i32 m0, s26, 3072
	s_nop 0
	global_load_lds_dwordx4 v2, s[32:33]
	s_add_i32 m0, s26, 4096
	s_nop 0
	global_load_lds_dwordx4 v2, s[34:35]
	s_add_i32 m0, s26, 5120
	s_nop 0
	global_load_lds_dwordx4 v2, s[36:37]
	s_add_i32 m0, s26, 6144
	s_nop 0
	global_load_lds_dwordx4 v2, s[38:39]
	s_add_i32 m0, s26, 7168
	s_nop 0
	global_load_lds_dwordx4 v2, s[40:41]
	s_add_i32 m0, s26, 8192
	s_nop 0
	global_load_lds_dwordx4 v2, s[42:43]
	s_add_i32 m0, s26, 30656
	s_nop 0
	global_load_lds_dwordx4 v2, s[30:31] offset:64
	s_add_i32 m0, s26, 31680
	s_nop 0
	global_load_lds_dwordx4 v2, s[32:33] offset:64
	s_add_i32 m0, s26, 32704
	s_nop 0
	global_load_lds_dwordx4 v2, s[34:35] offset:64
	s_add_i32 m0, s26, 33728
	s_nop 0
	global_load_lds_dwordx4 v2, s[36:37] offset:64
	s_add_i32 m0, s26, 34752
	s_nop 0
	global_load_lds_dwordx4 v2, s[38:39] offset:64
	s_add_i32 m0, s26, 35776
	s_nop 0
	global_load_lds_dwordx4 v2, s[40:41] offset:64
	s_add_i32 m0, s26, 36800
	s_nop 0
	global_load_lds_dwordx4 v2, s[42:43] offset:64
	s_add_i32 m0, s26, 59264
	s_nop 0
	global_load_lds_dwordx4 v2, s[30:31] offset:128
	s_add_i32 m0, s26, 60288
	s_nop 0
	global_load_lds_dwordx4 v2, s[32:33] offset:128
	s_add_i32 m0, s26, 61312
	s_nop 0
	global_load_lds_dwordx4 v2, s[34:35] offset:128
	s_add_i32 m0, s26, 62336
	s_nop 0
	global_load_lds_dwordx4 v2, s[36:37] offset:128
	s_add_i32 m0, s26, 63360
	s_nop 0
	global_load_lds_dwordx4 v2, s[38:39] offset:128
	s_add_i32 m0, s26, 64384
	s_nop 0
	global_load_lds_dwordx4 v2, s[40:41] offset:128
	s_add_i32 m0, s26, 65408
	s_nop 0
	global_load_lds_dwordx4 v2, s[42:43] offset:128
	s_add_i32 m0, s26, 87872
	s_nop 0
	global_load_lds_dwordx4 v2, s[30:31] offset:192
	s_add_i32 m0, s26, 88896
	s_nop 0
	global_load_lds_dwordx4 v2, s[32:33] offset:192
	s_add_i32 m0, s26, 89920
	s_nop 0
	global_load_lds_dwordx4 v2, s[34:35] offset:192
	s_add_i32 m0, s26, 90944
	s_nop 0
	global_load_lds_dwordx4 v2, s[36:37] offset:192
	s_add_i32 m0, s26, 91968
	s_nop 0
	global_load_lds_dwordx4 v2, s[38:39] offset:192
	s_add_i32 m0, s26, 92992
	s_nop 0
	global_load_lds_dwordx4 v2, s[40:41] offset:192
	s_add_i32 m0, s26, 94016
	s_nop 0
	global_load_lds_dwordx4 v2, s[42:43] offset:192
	s_waitcnt vmcnt(21)
	v_mul_f32_e32 v20, s29, v20
	ds_write_b32 v21, v20
	s_waitcnt lgkmcnt(0)
	s_barrier
	s_add_i32 m0, s26, 116480
	s_nop 0
	global_load_lds_dwordx4 v2, s[30:31] offset:256
	s_add_i32 m0, s26, 117504
	s_nop 0
	global_load_lds_dwordx4 v2, s[32:33] offset:256
	s_add_i32 m0, s26, 118528
	s_nop 0
	global_load_lds_dwordx4 v2, s[34:35] offset:256
	s_add_i32 m0, s26, 119552
	s_nop 0
	global_load_lds_dwordx4 v2, s[36:37] offset:256
	s_add_i32 m0, s26, 120576
	s_nop 0
	global_load_lds_dwordx4 v2, s[38:39] offset:256
	s_add_i32 m0, s26, 121600
	s_nop 0
	global_load_lds_dwordx4 v2, s[40:41] offset:256
	s_add_i32 m0, s26, 122624
	s_nop 0
	global_load_lds_dwordx4 v2, s[42:43] offset:256
	s_waitcnt vmcnt(21)
	s_barrier
	s_add_i32 m0, s26, 1728
	s_nop 0
	global_load_lds_dwordx4 v2, s[30:31] offset:320
	s_add_i32 m0, s26, 2752
	s_nop 0
	global_load_lds_dwordx4 v2, s[32:33] offset:320
	s_add_i32 m0, s26, 3776
	s_nop 0
	global_load_lds_dwordx4 v2, s[34:35] offset:320
	s_add_i32 m0, s26, 4800
	s_nop 0
	global_load_lds_dwordx4 v2, s[36:37] offset:320
	s_add_i32 m0, s26, 5824
	s_nop 0
	global_load_lds_dwordx4 v2, s[38:39] offset:320
	s_add_i32 m0, s26, 6848
	s_nop 0
	global_load_lds_dwordx4 v2, s[40:41] offset:320
	s_add_i32 m0, s26, 7872
	s_nop 0
	global_load_lds_dwordx4 v2, s[42:43] offset:320
	s_waitcnt vmcnt(21)
	s_barrier
	s_add_i32 m0, s26, 30336
	s_nop 0
	global_load_lds_dwordx4 v2, s[30:31] offset:384
	s_add_i32 m0, s26, 31360
	s_nop 0
	global_load_lds_dwordx4 v2, s[32:33] offset:384
	s_add_i32 m0, s26, 32384
	s_nop 0
	global_load_lds_dwordx4 v2, s[34:35] offset:384
	s_add_i32 m0, s26, 33408
	s_nop 0
	global_load_lds_dwordx4 v2, s[36:37] offset:384
	s_add_i32 m0, s26, 34432
	s_nop 0
	global_load_lds_dwordx4 v2, s[38:39] offset:384
	s_add_i32 m0, s26, 35456
	s_nop 0
	global_load_lds_dwordx4 v2, s[40:41] offset:384
	s_add_i32 m0, s26, 36480
	s_nop 0
	global_load_lds_dwordx4 v2, s[42:43] offset:384
	s_waitcnt vmcnt(21)
	s_barrier
	s_add_i32 m0, s26, 58944
	s_nop 0
	global_load_lds_dwordx4 v2, s[30:31] offset:448
	s_add_i32 m0, s26, 59968
	s_nop 0
	global_load_lds_dwordx4 v2, s[32:33] offset:448
	s_add_i32 m0, s26, 60992
	s_nop 0
	global_load_lds_dwordx4 v2, s[34:35] offset:448
	s_add_i32 m0, s26, 62016
	s_nop 0
	global_load_lds_dwordx4 v2, s[36:37] offset:448
	s_add_i32 m0, s26, 63040
	s_nop 0
	global_load_lds_dwordx4 v2, s[38:39] offset:448
	s_add_i32 m0, s26, 64064
	s_nop 0
	global_load_lds_dwordx4 v2, s[40:41] offset:448
	s_add_i32 m0, s26, 65088
	s_nop 0
	global_load_lds_dwordx4 v2, s[42:43] offset:448
	s_waitcnt vmcnt(21)
	s_barrier
	s_add_i32 m0, s26, 87552
	s_nop 0
	global_load_lds_dwordx4 v2, s[30:31] offset:512
	s_add_i32 m0, s26, 88576
	s_nop 0
	global_load_lds_dwordx4 v2, s[32:33] offset:512
	s_add_i32 m0, s26, 89600
	s_nop 0
	global_load_lds_dwordx4 v2, s[34:35] offset:512
	s_add_i32 m0, s26, 90624
	s_nop 0
	global_load_lds_dwordx4 v2, s[36:37] offset:512
	s_add_i32 m0, s26, 91648
	s_nop 0
	global_load_lds_dwordx4 v2, s[38:39] offset:512
	s_add_i32 m0, s26, 92672
	s_nop 0
	global_load_lds_dwordx4 v2, s[40:41] offset:512
	s_add_i32 m0, s26, 93696
	s_nop 0
	global_load_lds_dwordx4 v2, s[42:43] offset:512
	s_waitcnt vmcnt(21)
	s_barrier
	s_add_i32 m0, s26, 116160
	s_nop 0
	global_load_lds_dwordx4 v2, s[30:31] offset:576
	s_add_i32 m0, s26, 117184
	s_nop 0
	global_load_lds_dwordx4 v2, s[32:33] offset:576
	s_add_i32 m0, s26, 118208
	s_nop 0
	global_load_lds_dwordx4 v2, s[34:35] offset:576
	s_add_i32 m0, s26, 119232
	s_nop 0
	global_load_lds_dwordx4 v2, s[36:37] offset:576
	s_add_i32 m0, s26, 120256
	s_nop 0
	global_load_lds_dwordx4 v2, s[38:39] offset:576
	s_add_i32 m0, s26, 121280
	s_nop 0
	global_load_lds_dwordx4 v2, s[40:41] offset:576
	s_add_i32 m0, s26, 122304
	s_nop 0
	global_load_lds_dwordx4 v2, s[42:43] offset:576
	s_waitcnt vmcnt(21)
	s_barrier
	s_add_i32 m0, s26, 1408
	s_nop 0
	global_load_lds_dwordx4 v2, s[30:31] offset:640
	s_add_i32 m0, s26, 2432
	s_nop 0
	global_load_lds_dwordx4 v2, s[32:33] offset:640
	s_add_i32 m0, s26, 3456
	s_nop 0
	global_load_lds_dwordx4 v2, s[34:35] offset:640
	s_add_i32 m0, s26, 4480
	s_nop 0
	global_load_lds_dwordx4 v2, s[36:37] offset:640
	s_add_i32 m0, s26, 5504
	s_nop 0
	global_load_lds_dwordx4 v2, s[38:39] offset:640
	s_add_i32 m0, s26, 6528
	s_nop 0
	global_load_lds_dwordx4 v2, s[40:41] offset:640
	s_add_i32 m0, s26, 7552
	s_nop 0
	global_load_lds_dwordx4 v2, s[42:43] offset:640
	s_waitcnt vmcnt(21)
	s_barrier
	s_add_i32 m0, s26, 30016
	s_nop 0
	global_load_lds_dwordx4 v2, s[30:31] offset:704
	s_add_i32 m0, s26, 31040
	s_nop 0
	global_load_lds_dwordx4 v2, s[32:33] offset:704
	s_add_i32 m0, s26, 32064
	s_nop 0
	global_load_lds_dwordx4 v2, s[34:35] offset:704
	s_add_i32 m0, s26, 33088
	s_nop 0
	global_load_lds_dwordx4 v2, s[36:37] offset:704
	s_add_i32 m0, s26, 34112
	s_nop 0
	global_load_lds_dwordx4 v2, s[38:39] offset:704
	s_add_i32 m0, s26, 35136
	s_nop 0
	global_load_lds_dwordx4 v2, s[40:41] offset:704
	s_add_i32 m0, s26, 36160
	s_nop 0
	global_load_lds_dwordx4 v2, s[42:43] offset:704
	s_waitcnt vmcnt(21)
	s_barrier
	s_add_i32 m0, s26, 58624
	s_nop 0
	global_load_lds_dwordx4 v2, s[30:31] offset:768
	s_add_i32 m0, s26, 59648
	s_nop 0
	global_load_lds_dwordx4 v2, s[32:33] offset:768
	s_add_i32 m0, s26, 60672
	s_nop 0
	global_load_lds_dwordx4 v2, s[34:35] offset:768
	s_add_i32 m0, s26, 61696
	s_nop 0
	global_load_lds_dwordx4 v2, s[36:37] offset:768
	s_add_i32 m0, s26, 62720
	s_nop 0
	global_load_lds_dwordx4 v2, s[38:39] offset:768
	s_add_i32 m0, s26, 63744
	s_nop 0
	global_load_lds_dwordx4 v2, s[40:41] offset:768
	s_add_i32 m0, s26, 64768
	s_nop 0
	global_load_lds_dwordx4 v2, s[42:43] offset:768
	s_waitcnt vmcnt(21)
	s_barrier
	s_add_i32 m0, s26, 87232
	s_nop 0
	global_load_lds_dwordx4 v2, s[30:31] offset:832
	s_add_i32 m0, s26, 88256
	s_nop 0
	global_load_lds_dwordx4 v2, s[32:33] offset:832
	s_add_i32 m0, s26, 89280
	s_nop 0
	global_load_lds_dwordx4 v2, s[34:35] offset:832
	s_add_i32 m0, s26, 90304
	s_nop 0
	global_load_lds_dwordx4 v2, s[36:37] offset:832
	s_add_i32 m0, s26, 91328
	s_nop 0
	global_load_lds_dwordx4 v2, s[38:39] offset:832
	s_add_i32 m0, s26, 92352
	s_nop 0
	global_load_lds_dwordx4 v2, s[40:41] offset:832
	s_add_i32 m0, s26, 93376
	s_nop 0
	global_load_lds_dwordx4 v2, s[42:43] offset:832
	s_waitcnt vmcnt(21)
	s_barrier
	s_add_i32 m0, s26, 115840
	s_nop 0
	global_load_lds_dwordx4 v2, s[30:31] offset:896
	s_add_i32 m0, s26, 116864
	s_nop 0
	global_load_lds_dwordx4 v2, s[32:33] offset:896
	s_add_i32 m0, s26, 117888
	s_nop 0
	global_load_lds_dwordx4 v2, s[34:35] offset:896
	s_add_i32 m0, s26, 118912
	s_nop 0
	global_load_lds_dwordx4 v2, s[36:37] offset:896
	s_add_i32 m0, s26, 119936
	s_nop 0
	global_load_lds_dwordx4 v2, s[38:39] offset:896
	s_add_i32 m0, s26, 120960
	s_nop 0
	global_load_lds_dwordx4 v2, s[40:41] offset:896
	s_add_i32 m0, s26, 121984
	s_nop 0
	global_load_lds_dwordx4 v2, s[42:43] offset:896
	s_waitcnt vmcnt(21)
	s_barrier
	s_add_i32 m0, s26, 1088
	s_nop 0
	global_load_lds_dwordx4 v2, s[30:31] offset:960
	s_add_i32 m0, s26, 2112
	s_nop 0
	global_load_lds_dwordx4 v2, s[32:33] offset:960
	s_add_i32 m0, s26, 3136
	s_nop 0
	global_load_lds_dwordx4 v2, s[34:35] offset:960
	s_add_i32 m0, s26, 4160
	s_nop 0
	global_load_lds_dwordx4 v2, s[36:37] offset:960
	s_add_i32 m0, s26, 5184
	s_nop 0
	global_load_lds_dwordx4 v2, s[38:39] offset:960
	s_add_i32 m0, s26, 6208
	s_nop 0
	global_load_lds_dwordx4 v2, s[40:41] offset:960
	s_add_i32 m0, s26, 7232
	s_nop 0
	global_load_lds_dwordx4 v2, s[42:43] offset:960
	s_waitcnt vmcnt(21)
	s_barrier
	s_add_i32 m0, s26, 29696
	s_nop 0
	global_load_lds_dwordx4 v2, s[30:31] offset:1024
	s_add_i32 m0, s26, 30720
	s_nop 0
	global_load_lds_dwordx4 v2, s[32:33] offset:1024
	s_add_i32 m0, s26, 31744
	s_nop 0
	global_load_lds_dwordx4 v2, s[34:35] offset:1024
	s_add_i32 m0, s26, 32768
	s_nop 0
	global_load_lds_dwordx4 v2, s[36:37] offset:1024
	s_add_i32 m0, s26, 33792
	s_nop 0
	global_load_lds_dwordx4 v2, s[38:39] offset:1024
	s_add_i32 m0, s26, 34816
	s_nop 0
	global_load_lds_dwordx4 v2, s[40:41] offset:1024
	s_add_i32 m0, s26, 35840
	s_nop 0
	global_load_lds_dwordx4 v2, s[42:43] offset:1024
	s_waitcnt vmcnt(21)
	s_barrier
	s_add_i32 m0, s26, 58304
	s_nop 0
	global_load_lds_dwordx4 v2, s[30:31] offset:1088
	s_add_i32 m0, s26, 59328
	s_nop 0
	global_load_lds_dwordx4 v2, s[32:33] offset:1088
	s_add_i32 m0, s26, 60352
	s_nop 0
	global_load_lds_dwordx4 v2, s[34:35] offset:1088
	s_add_i32 m0, s26, 61376
	s_nop 0
	global_load_lds_dwordx4 v2, s[36:37] offset:1088
	s_add_i32 m0, s26, 62400
	s_nop 0
	global_load_lds_dwordx4 v2, s[38:39] offset:1088
	s_add_i32 m0, s26, 63424
	s_nop 0
	global_load_lds_dwordx4 v2, s[40:41] offset:1088
	s_add_i32 m0, s26, 64448
	s_nop 0
	global_load_lds_dwordx4 v2, s[42:43] offset:1088
	s_waitcnt vmcnt(21)
	s_barrier
	s_add_i32 m0, s26, 86912
	s_nop 0
	global_load_lds_dwordx4 v2, s[30:31] offset:1152
	s_add_i32 m0, s26, 87936
	s_nop 0
	global_load_lds_dwordx4 v2, s[32:33] offset:1152
	s_add_i32 m0, s26, 88960
	s_nop 0
	global_load_lds_dwordx4 v2, s[34:35] offset:1152
	s_add_i32 m0, s26, 89984
	s_nop 0
	global_load_lds_dwordx4 v2, s[36:37] offset:1152
	s_add_i32 m0, s26, 91008
	s_nop 0
	global_load_lds_dwordx4 v2, s[38:39] offset:1152
	s_add_i32 m0, s26, 92032
	s_nop 0
	global_load_lds_dwordx4 v2, s[40:41] offset:1152
	s_add_i32 m0, s26, 93056
	s_nop 0
	global_load_lds_dwordx4 v2, s[42:43] offset:1152
	s_waitcnt vmcnt(21)
	s_barrier
	s_add_i32 m0, s26, 115520
	s_nop 0
	global_load_lds_dwordx4 v2, s[30:31] offset:1216
	s_add_i32 m0, s26, 116544
	s_nop 0
	global_load_lds_dwordx4 v2, s[32:33] offset:1216
	s_add_i32 m0, s26, 117568
	s_nop 0
	global_load_lds_dwordx4 v2, s[34:35] offset:1216
	s_add_i32 m0, s26, 118592
	s_nop 0
	global_load_lds_dwordx4 v2, s[36:37] offset:1216
	s_add_i32 m0, s26, 119616
	s_nop 0
	global_load_lds_dwordx4 v2, s[38:39] offset:1216
	s_add_i32 m0, s26, 120640
	s_nop 0
	global_load_lds_dwordx4 v2, s[40:41] offset:1216
	s_add_i32 m0, s26, 121664
	s_nop 0
	global_load_lds_dwordx4 v2, s[42:43] offset:1216
	s_waitcnt vmcnt(21)
	s_barrier
	s_add_i32 m0, s26, 768
	s_nop 0
	global_load_lds_dwordx4 v2, s[30:31] offset:1280
	s_add_i32 m0, s26, 1792
	s_nop 0
	global_load_lds_dwordx4 v2, s[32:33] offset:1280
	s_add_i32 m0, s26, 2816
	s_nop 0
	global_load_lds_dwordx4 v2, s[34:35] offset:1280
	s_add_i32 m0, s26, 3840
	s_nop 0
	global_load_lds_dwordx4 v2, s[36:37] offset:1280
	s_add_i32 m0, s26, 4864
	s_nop 0
	global_load_lds_dwordx4 v2, s[38:39] offset:1280
	s_add_i32 m0, s26, 5888
	s_nop 0
	global_load_lds_dwordx4 v2, s[40:41] offset:1280
	s_add_i32 m0, s26, 6912
	s_nop 0
	global_load_lds_dwordx4 v2, s[42:43] offset:1280
	s_waitcnt vmcnt(21)
	s_barrier
	s_add_i32 m0, s26, 29376
	s_nop 0
	global_load_lds_dwordx4 v2, s[30:31] offset:1344
	s_add_i32 m0, s26, 30400
	s_nop 0
	global_load_lds_dwordx4 v2, s[32:33] offset:1344
	s_add_i32 m0, s26, 31424
	s_nop 0
	global_load_lds_dwordx4 v2, s[34:35] offset:1344
	s_add_i32 m0, s26, 32448
	s_nop 0
	global_load_lds_dwordx4 v2, s[36:37] offset:1344
	s_add_i32 m0, s26, 33472
	s_nop 0
	global_load_lds_dwordx4 v2, s[38:39] offset:1344
	s_add_i32 m0, s26, 34496
	s_nop 0
	global_load_lds_dwordx4 v2, s[40:41] offset:1344
	s_add_i32 m0, s26, 35520
	s_nop 0
	global_load_lds_dwordx4 v2, s[42:43] offset:1344
	s_waitcnt vmcnt(21)
	s_barrier
	s_add_i32 m0, s26, 57984
	s_nop 0
	global_load_lds_dwordx4 v2, s[30:31] offset:1408
	s_add_i32 m0, s26, 59008
	s_nop 0
	global_load_lds_dwordx4 v2, s[32:33] offset:1408
	s_add_i32 m0, s26, 60032
	s_nop 0
	global_load_lds_dwordx4 v2, s[34:35] offset:1408
	s_add_i32 m0, s26, 61056
	s_nop 0
	global_load_lds_dwordx4 v2, s[36:37] offset:1408
	s_add_i32 m0, s26, 62080
	s_nop 0
	global_load_lds_dwordx4 v2, s[38:39] offset:1408
	s_add_i32 m0, s26, 63104
	s_nop 0
	global_load_lds_dwordx4 v2, s[40:41] offset:1408
	s_add_i32 m0, s26, 64128
	s_nop 0
	global_load_lds_dwordx4 v2, s[42:43] offset:1408
	s_waitcnt vmcnt(21)
	s_barrier
	s_add_i32 m0, s26, 86592
	s_nop 0
	global_load_lds_dwordx4 v2, s[30:31] offset:1472
	s_add_i32 m0, s26, 87616
	s_nop 0
	global_load_lds_dwordx4 v2, s[32:33] offset:1472
	s_add_i32 m0, s26, 88640
	s_nop 0
	global_load_lds_dwordx4 v2, s[34:35] offset:1472
	s_add_i32 m0, s26, 89664
	s_nop 0
	global_load_lds_dwordx4 v2, s[36:37] offset:1472
	s_add_i32 m0, s26, 90688
	s_nop 0
	global_load_lds_dwordx4 v2, s[38:39] offset:1472
	s_add_i32 m0, s26, 91712
	s_nop 0
	global_load_lds_dwordx4 v2, s[40:41] offset:1472
	s_add_i32 m0, s26, 92736
	s_nop 0
	global_load_lds_dwordx4 v2, s[42:43] offset:1472
	s_waitcnt vmcnt(21)
	s_barrier
	s_waitcnt vmcnt(14)
	s_barrier
	s_waitcnt vmcnt(7)
	s_barrier
	s_waitcnt vmcnt(0)
	s_barrier
.LBB1_30:
	s_setprio 0
	s_load_dwordx8 s[8:15], s[0:1], 0x10
	s_load_dwordx2 s[16:17], s[0:1], 0x30
	s_bitcmp1_b32 s18, 6
	s_cselect_b32 s24, 0x60, 0
	s_lshr_b32 s4, s18, 1
	s_and_b32 s23, s4, 0x7fffffc0
	v_lshrrev_b32_e32 v98, 5, v1
	s_cmpk_lt_u32 s18, 0x200
	v_and_b32_e32 v1, 31, v0
	v_mov_b32_e32 v2, 0
	s_cselect_b64 s[4:5], -1, 0
	s_cmpk_gt_u32 s18, 0x1ff
	v_mov_b32_e32 v3, 0
	v_mov_b32_e32 v4, 0
	v_mov_b32_e32 v5, 0
	v_mov_b32_e32 v6, 0
	v_mov_b32_e32 v7, 0
	v_mov_b32_e32 v8, 0
	v_mov_b32_e32 v9, 0
	v_mov_b32_e32 v10, 0
	v_mov_b32_e32 v11, 0
	v_mov_b32_e32 v12, 0
	v_mov_b32_e32 v13, 0
	v_mov_b32_e32 v14, 0
	v_mov_b32_e32 v15, 0
	v_mov_b32_e32 v16, 0
	v_mov_b32_e32 v17, 0
	v_mov_b32_e32 v50, 0
	v_mov_b32_e32 v51, 0
	v_mov_b32_e32 v52, 0
	v_mov_b32_e32 v53, 0
	v_mov_b32_e32 v54, 0
	v_mov_b32_e32 v55, 0
	v_mov_b32_e32 v56, 0
	v_mov_b32_e32 v57, 0
	v_mov_b32_e32 v58, 0
	v_mov_b32_e32 v59, 0
	v_mov_b32_e32 v60, 0
	v_mov_b32_e32 v61, 0
	v_mov_b32_e32 v62, 0
	v_mov_b32_e32 v63, 0
	v_mov_b32_e32 v64, 0
	v_mov_b32_e32 v65, 0
	v_mov_b32_e32 v18, 0
	v_mov_b32_e32 v19, 0
	v_mov_b32_e32 v20, 0
	v_mov_b32_e32 v21, 0
	v_mov_b32_e32 v22, 0
	v_mov_b32_e32 v23, 0
	v_mov_b32_e32 v24, 0
	v_mov_b32_e32 v25, 0
	v_mov_b32_e32 v26, 0
	v_mov_b32_e32 v27, 0
	v_mov_b32_e32 v28, 0
	v_mov_b32_e32 v29, 0
	v_mov_b32_e32 v30, 0
	v_mov_b32_e32 v31, 0
	v_mov_b32_e32 v32, 0
	v_mov_b32_e32 v33, 0
	v_mov_b32_e32 v66, 0
	v_mov_b32_e32 v67, 0
	v_mov_b32_e32 v68, 0
	v_mov_b32_e32 v69, 0
	v_mov_b32_e32 v70, 0
	v_mov_b32_e32 v71, 0
	v_mov_b32_e32 v72, 0
	v_mov_b32_e32 v73, 0
	v_mov_b32_e32 v74, 0
	v_mov_b32_e32 v75, 0
	v_mov_b32_e32 v76, 0
	v_mov_b32_e32 v77, 0
	v_mov_b32_e32 v78, 0
	v_mov_b32_e32 v79, 0
	v_mov_b32_e32 v80, 0
	v_mov_b32_e32 v81, 0
	v_mov_b32_e32 v34, 0
	v_mov_b32_e32 v35, 0
	v_mov_b32_e32 v36, 0
	v_mov_b32_e32 v37, 0
	v_mov_b32_e32 v38, 0
	v_mov_b32_e32 v39, 0
	v_mov_b32_e32 v40, 0
	v_mov_b32_e32 v41, 0
	v_mov_b32_e32 v42, 0
	v_mov_b32_e32 v43, 0
	v_mov_b32_e32 v44, 0
	v_mov_b32_e32 v45, 0
	v_mov_b32_e32 v46, 0
	v_mov_b32_e32 v47, 0
	v_mov_b32_e32 v48, 0
	v_mov_b32_e32 v49, 0
	v_mov_b32_e32 v82, 0
	v_mov_b32_e32 v83, 0
	v_mov_b32_e32 v84, 0
	v_mov_b32_e32 v85, 0
	v_mov_b32_e32 v86, 0
	v_mov_b32_e32 v87, 0
	v_mov_b32_e32 v88, 0
	v_mov_b32_e32 v89, 0
	v_mov_b32_e32 v90, 0
	v_mov_b32_e32 v91, 0
	v_mov_b32_e32 v92, 0
	v_mov_b32_e32 v93, 0
	v_mov_b32_e32 v94, 0
	v_mov_b32_e32 v95, 0
	v_mov_b32_e32 v96, 0
	v_mov_b32_e32 v97, 0
	v_or_b32_e32 v99, s24, v1
	v_or_b32_e32 v100, s23, v1
	s_cbranch_scc1 .LBB1_35
	v_bfe_u32 v109, v0, 2, 2
	v_xor_b32_e32 v110, v109, v98
	v_xor_b32_e32 v111, 2, v110
	v_lshlrev_b32_e32 v110, 4, v110
	v_lshlrev_b32_e32 v111, 4, v111
	v_lshl_add_u32 v101, v99, 6, v110
	v_lshl_add_u32 v102, v99, 6, v111
	v_lshl_add_u32 v103, v100, 6, v110
	v_lshl_add_u32 v104, v100, 6, v111
	v_add_u32_e32 v101, 0x800, v101
	v_add_u32_e32 v102, 0x800, v102
	v_add_u32_e32 v103, 0x3800, v103
	v_add_u32_e32 v104, 0x3800, v104
	v_add_u32_e32 v105, 0xe000, v101
	v_add_u32_e32 v106, 0xe000, v102
	v_add_u32_e32 v107, 0xe000, v103
	v_add_u32_e32 v108, 0xe000, v104
	v_add_u32_e32 v152, 0x1c000, v101
	v_add_u32_e32 v153, 0x1c000, v102
	v_add_u32_e32 v154, 0x1c000, v103
	v_add_u32_e32 v155, 0x1c000, v104
	s_cmp_lt_u32 s2, 64
	s_cbranch_scc1 .Lqkv_cv
	s_barrier
	ds_read_b128 v[124:127], v103
	ds_read_b128 v[112:115], v101
	ds_read_b128 v[128:131], v103 offset:2048
	ds_read_b128 v[116:119], v101 offset:2048
	ds_read_b128 v[120:123], v101 offset:4096
	s_waitcnt lgkmcnt(0)
	v_mfma_f32_32x32x16_f16 v[82:97], v[112:115], v[124:127], v[82:97]
	ds_read_b128 v[144:147], v104
	ds_read_b128 v[132:135], v102
	v_mfma_f32_32x32x16_f16 v[34:49], v[112:115], v[128:131], v[34:49]
	ds_read_b128 v[148:151], v104 offset:2048
	ds_read_b128 v[136:139], v102 offset:2048
	v_mfma_f32_32x32x16_f16 v[66:81], v[116:119], v[124:127], v[66:81]
	ds_read_b128 v[140:143], v102 offset:4096
	v_mfma_f32_32x32x16_f16 v[18:33], v[116:119], v[128:131], v[18:33]
	v_mfma_f32_32x32x16_f16 v[50:65], v[120:123], v[124:127], v[50:65]
	v_mfma_f32_32x32x16_f16 v[2:17], v[120:123], v[128:131], v[2:17]
	s_waitcnt lgkmcnt(0)
	s_barrier
	v_mfma_f32_32x32x16_f16 v[82:97], v[132:135], v[144:147], v[82:97]
	ds_read_b128 v[124:127], v103 offset:28672
	ds_read_b128 v[112:115], v101 offset:28672
	v_mfma_f32_32x32x16_f16 v[34:49], v[132:135], v[148:151], v[34:49]
	ds_read_b128 v[128:131], v103 offset:30720
	ds_read_b128 v[116:119], v101 offset:30720
	v_mfma_f32_32x32x16_f16 v[66:81], v[136:139], v[144:147], v[66:81]
	ds_read_b128 v[120:123], v101 offset:32768
	v_mfma_f32_32x32x16_f16 v[18:33], v[136:139], v[148:151], v[18:33]
	v_mfma_f32_32x32x16_f16 v[50:65], v[140:143], v[144:147], v[50:65]
	v_mfma_f32_32x32x16_f16 v[2:17], v[140:143], v[148:151], v[2:17]
	s_waitcnt lgkmcnt(0)
	v_mfma_f32_32x32x16_f16 v[82:97], v[112:115], v[124:127], v[82:97]
	ds_read_b128 v[144:147], v104 offset:28672
	ds_read_b128 v[132:135], v102 offset:28672
	v_mfma_f32_32x32x16_f16 v[34:49], v[112:115], v[128:131], v[34:49]
	ds_read_b128 v[148:151], v104 offset:30720
	ds_read_b128 v[136:139], v102 offset:30720
	v_mfma_f32_32x32x16_f16 v[66:81], v[116:119], v[124:127], v[66:81]
	ds_read_b128 v[140:143], v102 offset:32768
	v_mfma_f32_32x32x16_f16 v[18:33], v[116:119], v[128:131], v[18:33]
	v_mfma_f32_32x32x16_f16 v[50:65], v[120:123], v[124:127], v[50:65]
	v_mfma_f32_32x32x16_f16 v[2:17], v[120:123], v[128:131], v[2:17]
	s_waitcnt lgkmcnt(0)
	s_barrier
	v_mfma_f32_32x32x16_f16 v[82:97], v[132:135], v[144:147], v[82:97]
	ds_read_b128 v[124:127], v107
	ds_read_b128 v[112:115], v105
	v_mfma_f32_32x32x16_f16 v[34:49], v[132:135], v[148:151], v[34:49]
	ds_read_b128 v[128:131], v107 offset:2048
	ds_read_b128 v[116:119], v105 offset:2048
	v_mfma_f32_32x32x16_f16 v[66:81], v[136:139], v[144:147], v[66:81]
	ds_read_b128 v[120:123], v105 offset:4096
	v_mfma_f32_32x32x16_f16 v[18:33], v[136:139], v[148:151], v[18:33]
	v_mfma_f32_32x32x16_f16 v[50:65], v[140:143], v[144:147], v[50:65]
	v_mfma_f32_32x32x16_f16 v[2:17], v[140:143], v[148:151], v[2:17]
	s_waitcnt lgkmcnt(0)
	v_mfma_f32_32x32x16_f16 v[82:97], v[112:115], v[124:127], v[82:97]
	ds_read_b128 v[144:147], v108
	ds_read_b128 v[132:135], v106
	v_mfma_f32_32x32x16_f16 v[34:49], v[112:115], v[128:131], v[34:49]
	ds_read_b128 v[148:151], v108 offset:2048
	ds_read_b128 v[136:139], v106 offset:2048
	v_mfma_f32_32x32x16_f16 v[66:81], v[116:119], v[124:127], v[66:81]
	ds_read_b128 v[140:143], v106 offset:4096
	v_mfma_f32_32x32x16_f16 v[18:33], v[116:119], v[128:131], v[18:33]
	v_mfma_f32_32x32x16_f16 v[50:65], v[120:123], v[124:127], v[50:65]
	v_mfma_f32_32x32x16_f16 v[2:17], v[120:123], v[128:131], v[2:17]
	s_waitcnt lgkmcnt(0)
	s_barrier
	v_mfma_f32_32x32x16_f16 v[82:97], v[132:135], v[144:147], v[82:97]
	ds_read_b128 v[124:127], v107 offset:28672
	ds_read_b128 v[112:115], v105 offset:28672
	v_mfma_f32_32x32x16_f16 v[34:49], v[132:135], v[148:151], v[34:49]
	ds_read_b128 v[128:131], v107 offset:30720
	ds_read_b128 v[116:119], v105 offset:30720
	v_mfma_f32_32x32x16_f16 v[66:81], v[136:139], v[144:147], v[66:81]
	ds_read_b128 v[120:123], v105 offset:32768
	v_mfma_f32_32x32x16_f16 v[18:33], v[136:139], v[148:151], v[18:33]
	v_mfma_f32_32x32x16_f16 v[50:65], v[140:143], v[144:147], v[50:65]
	v_mfma_f32_32x32x16_f16 v[2:17], v[140:143], v[148:151], v[2:17]
	s_waitcnt lgkmcnt(0)
	v_mfma_f32_32x32x16_f16 v[82:97], v[112:115], v[124:127], v[82:97]
	ds_read_b128 v[144:147], v108 offset:28672
	ds_read_b128 v[132:135], v106 offset:28672
	v_mfma_f32_32x32x16_f16 v[34:49], v[112:115], v[128:131], v[34:49]
	ds_read_b128 v[148:151], v108 offset:30720
	ds_read_b128 v[136:139], v106 offset:30720
	v_mfma_f32_32x32x16_f16 v[66:81], v[116:119], v[124:127], v[66:81]
	ds_read_b128 v[140:143], v106 offset:32768
	v_mfma_f32_32x32x16_f16 v[18:33], v[116:119], v[128:131], v[18:33]
	v_mfma_f32_32x32x16_f16 v[50:65], v[120:123], v[124:127], v[50:65]
	v_mfma_f32_32x32x16_f16 v[2:17], v[120:123], v[128:131], v[2:17]
	s_waitcnt lgkmcnt(0)
	s_barrier
	v_mfma_f32_32x32x16_f16 v[82:97], v[132:135], v[144:147], v[82:97]
	ds_read_b128 v[124:127], v154
	ds_read_b128 v[112:115], v152
	v_mfma_f32_32x32x16_f16 v[34:49], v[132:135], v[148:151], v[34:49]
	ds_read_b128 v[128:131], v154 offset:2048
	ds_read_b128 v[116:119], v152 offset:2048
	v_mfma_f32_32x32x16_f16 v[66:81], v[136:139], v[144:147], v[66:81]
	ds_read_b128 v[120:123], v152 offset:4096
	v_mfma_f32_32x32x16_f16 v[18:33], v[136:139], v[148:151], v[18:33]
	v_mfma_f32_32x32x16_f16 v[50:65], v[140:143], v[144:147], v[50:65]
	v_mfma_f32_32x32x16_f16 v[2:17], v[140:143], v[148:151], v[2:17]
	s_waitcnt lgkmcnt(0)
	v_mfma_f32_32x32x16_f16 v[82:97], v[112:115], v[124:127], v[82:97]
	ds_read_b128 v[144:147], v155
	ds_read_b128 v[132:135], v153
	v_mfma_f32_32x32x16_f16 v[34:49], v[112:115], v[128:131], v[34:49]
	ds_read_b128 v[148:151], v155 offset:2048
	ds_read_b128 v[136:139], v153 offset:2048
	v_mfma_f32_32x32x16_f16 v[66:81], v[116:119], v[124:127], v[66:81]
	ds_read_b128 v[140:143], v153 offset:4096
	v_mfma_f32_32x32x16_f16 v[18:33], v[116:119], v[128:131], v[18:33]
	v_mfma_f32_32x32x16_f16 v[50:65], v[120:123], v[124:127], v[50:65]
	v_mfma_f32_32x32x16_f16 v[2:17], v[120:123], v[128:131], v[2:17]
	s_waitcnt lgkmcnt(0)
	s_barrier
	v_mfma_f32_32x32x16_f16 v[82:97], v[132:135], v[144:147], v[82:97]
	ds_read_b128 v[124:127], v103
	ds_read_b128 v[112:115], v101
	v_mfma_f32_32x32x16_f16 v[34:49], v[132:135], v[148:151], v[34:49]
	ds_read_b128 v[128:131], v103 offset:2048
	ds_read_b128 v[116:119], v101 offset:2048
	v_mfma_f32_32x32x16_f16 v[66:81], v[136:139], v[144:147], v[66:81]
	ds_read_b128 v[120:123], v101 offset:4096
	v_mfma_f32_32x32x16_f16 v[18:33], v[136:139], v[148:151], v[18:33]
	v_mfma_f32_32x32x16_f16 v[50:65], v[140:143], v[144:147], v[50:65]
	v_mfma_f32_32x32x16_f16 v[2:17], v[140:143], v[148:151], v[2:17]
	s_waitcnt lgkmcnt(0)
	v_mfma_f32_32x32x16_f16 v[82:97], v[112:115], v[124:127], v[82:97]
	ds_read_b128 v[144:147], v104
	ds_read_b128 v[132:135], v102
	v_mfma_f32_32x32x16_f16 v[34:49], v[112:115], v[128:131], v[34:49]
	ds_read_b128 v[148:151], v104 offset:2048
	ds_read_b128 v[136:139], v102 offset:2048
	v_mfma_f32_32x32x16_f16 v[66:81], v[116:119], v[124:127], v[66:81]
	ds_read_b128 v[140:143], v102 offset:4096
	v_mfma_f32_32x32x16_f16 v[18:33], v[116:119], v[128:131], v[18:33]
	v_mfma_f32_32x32x16_f16 v[50:65], v[120:123], v[124:127], v[50:65]
	v_mfma_f32_32x32x16_f16 v[2:17], v[120:123], v[128:131], v[2:17]
	s_waitcnt lgkmcnt(0)
	s_barrier
	v_mfma_f32_32x32x16_f16 v[82:97], v[132:135], v[144:147], v[82:97]
	ds_read_b128 v[124:127], v103 offset:28672
	ds_read_b128 v[112:115], v101 offset:28672
	v_mfma_f32_32x32x16_f16 v[34:49], v[132:135], v[148:151], v[34:49]
	ds_read_b128 v[128:131], v103 offset:30720
	ds_read_b128 v[116:119], v101 offset:30720
	v_mfma_f32_32x32x16_f16 v[66:81], v[136:139], v[144:147], v[66:81]
	ds_read_b128 v[120:123], v101 offset:32768
	v_mfma_f32_32x32x16_f16 v[18:33], v[136:139], v[148:151], v[18:33]
	v_mfma_f32_32x32x16_f16 v[50:65], v[140:143], v[144:147], v[50:65]
	v_mfma_f32_32x32x16_f16 v[2:17], v[140:143], v[148:151], v[2:17]
	s_waitcnt lgkmcnt(0)
	v_mfma_f32_32x32x16_f16 v[82:97], v[112:115], v[124:127], v[82:97]
	ds_read_b128 v[144:147], v104 offset:28672
	ds_read_b128 v[132:135], v102 offset:28672
	v_mfma_f32_32x32x16_f16 v[34:49], v[112:115], v[128:131], v[34:49]
	ds_read_b128 v[148:151], v104 offset:30720
	ds_read_b128 v[136:139], v102 offset:30720
	v_mfma_f32_32x32x16_f16 v[66:81], v[116:119], v[124:127], v[66:81]
	ds_read_b128 v[140:143], v102 offset:32768
	v_mfma_f32_32x32x16_f16 v[18:33], v[116:119], v[128:131], v[18:33]
	v_mfma_f32_32x32x16_f16 v[50:65], v[120:123], v[124:127], v[50:65]
	v_mfma_f32_32x32x16_f16 v[2:17], v[120:123], v[128:131], v[2:17]
	s_waitcnt lgkmcnt(0)
	s_barrier
	v_mfma_f32_32x32x16_f16 v[82:97], v[132:135], v[144:147], v[82:97]
	ds_read_b128 v[124:127], v107
	ds_read_b128 v[112:115], v105
	v_mfma_f32_32x32x16_f16 v[34:49], v[132:135], v[148:151], v[34:49]
	ds_read_b128 v[128:131], v107 offset:2048
	ds_read_b128 v[116:119], v105 offset:2048
	v_mfma_f32_32x32x16_f16 v[66:81], v[136:139], v[144:147], v[66:81]
	ds_read_b128 v[120:123], v105 offset:4096
	v_mfma_f32_32x32x16_f16 v[18:33], v[136:139], v[148:151], v[18:33]
	v_mfma_f32_32x32x16_f16 v[50:65], v[140:143], v[144:147], v[50:65]
	v_mfma_f32_32x32x16_f16 v[2:17], v[140:143], v[148:151], v[2:17]
	s_waitcnt lgkmcnt(0)
	v_mfma_f32_32x32x16_f16 v[82:97], v[112:115], v[124:127], v[82:97]
	ds_read_b128 v[144:147], v108
	ds_read_b128 v[132:135], v106
	v_mfma_f32_32x32x16_f16 v[34:49], v[112:115], v[128:131], v[34:49]
	ds_read_b128 v[148:151], v108 offset:2048
	ds_read_b128 v[136:139], v106 offset:2048
	v_mfma_f32_32x32x16_f16 v[66:81], v[116:119], v[124:127], v[66:81]
	ds_read_b128 v[140:143], v106 offset:4096
	v_mfma_f32_32x32x16_f16 v[18:33], v[116:119], v[128:131], v[18:33]
	v_mfma_f32_32x32x16_f16 v[50:65], v[120:123], v[124:127], v[50:65]
	v_mfma_f32_32x32x16_f16 v[2:17], v[120:123], v[128:131], v[2:17]
	s_waitcnt lgkmcnt(0)
	s_barrier
	v_mfma_f32_32x32x16_f16 v[82:97], v[132:135], v[144:147], v[82:97]
	ds_read_b128 v[124:127], v107 offset:28672
	ds_read_b128 v[112:115], v105 offset:28672
	v_mfma_f32_32x32x16_f16 v[34:49], v[132:135], v[148:151], v[34:49]
	ds_read_b128 v[128:131], v107 offset:30720
	ds_read_b128 v[116:119], v105 offset:30720
	v_mfma_f32_32x32x16_f16 v[66:81], v[136:139], v[144:147], v[66:81]
	ds_read_b128 v[120:123], v105 offset:32768
	v_mfma_f32_32x32x16_f16 v[18:33], v[136:139], v[148:151], v[18:33]
	v_mfma_f32_32x32x16_f16 v[50:65], v[140:143], v[144:147], v[50:65]
	v_mfma_f32_32x32x16_f16 v[2:17], v[140:143], v[148:151], v[2:17]
	s_waitcnt lgkmcnt(0)
	v_mfma_f32_32x32x16_f16 v[82:97], v[112:115], v[124:127], v[82:97]
	ds_read_b128 v[144:147], v108 offset:28672
	ds_read_b128 v[132:135], v106 offset:28672
	v_mfma_f32_32x32x16_f16 v[34:49], v[112:115], v[128:131], v[34:49]
	ds_read_b128 v[148:151], v108 offset:30720
	ds_read_b128 v[136:139], v106 offset:30720
	v_mfma_f32_32x32x16_f16 v[66:81], v[116:119], v[124:127], v[66:81]
	ds_read_b128 v[140:143], v106 offset:32768
	v_mfma_f32_32x32x16_f16 v[18:33], v[116:119], v[128:131], v[18:33]
	v_mfma_f32_32x32x16_f16 v[50:65], v[120:123], v[124:127], v[50:65]
	v_mfma_f32_32x32x16_f16 v[2:17], v[120:123], v[128:131], v[2:17]
	s_waitcnt lgkmcnt(0)
	s_barrier
	v_mfma_f32_32x32x16_f16 v[82:97], v[132:135], v[144:147], v[82:97]
	ds_read_b128 v[124:127], v154
	ds_read_b128 v[112:115], v152
	v_mfma_f32_32x32x16_f16 v[34:49], v[132:135], v[148:151], v[34:49]
	ds_read_b128 v[128:131], v154 offset:2048
	ds_read_b128 v[116:119], v152 offset:2048
	v_mfma_f32_32x32x16_f16 v[66:81], v[136:139], v[144:147], v[66:81]
	ds_read_b128 v[120:123], v152 offset:4096
	v_mfma_f32_32x32x16_f16 v[18:33], v[136:139], v[148:151], v[18:33]
	v_mfma_f32_32x32x16_f16 v[50:65], v[140:143], v[144:147], v[50:65]
	v_mfma_f32_32x32x16_f16 v[2:17], v[140:143], v[148:151], v[2:17]
	s_waitcnt lgkmcnt(0)
	v_mfma_f32_32x32x16_f16 v[82:97], v[112:115], v[124:127], v[82:97]
	ds_read_b128 v[144:147], v155
	ds_read_b128 v[132:135], v153
	v_mfma_f32_32x32x16_f16 v[34:49], v[112:115], v[128:131], v[34:49]
	ds_read_b128 v[148:151], v155 offset:2048
	ds_read_b128 v[136:139], v153 offset:2048
	v_mfma_f32_32x32x16_f16 v[66:81], v[116:119], v[124:127], v[66:81]
	ds_read_b128 v[140:143], v153 offset:4096
	v_mfma_f32_32x32x16_f16 v[18:33], v[116:119], v[128:131], v[18:33]
	v_mfma_f32_32x32x16_f16 v[50:65], v[120:123], v[124:127], v[50:65]
	v_mfma_f32_32x32x16_f16 v[2:17], v[120:123], v[128:131], v[2:17]
	s_waitcnt lgkmcnt(0)
	s_barrier
	v_mfma_f32_32x32x16_f16 v[82:97], v[132:135], v[144:147], v[82:97]
	ds_read_b128 v[124:127], v103
	ds_read_b128 v[112:115], v101
	v_mfma_f32_32x32x16_f16 v[34:49], v[132:135], v[148:151], v[34:49]
	ds_read_b128 v[128:131], v103 offset:2048
	ds_read_b128 v[116:119], v101 offset:2048
	v_mfma_f32_32x32x16_f16 v[66:81], v[136:139], v[144:147], v[66:81]
	ds_read_b128 v[120:123], v101 offset:4096
	v_mfma_f32_32x32x16_f16 v[18:33], v[136:139], v[148:151], v[18:33]
	v_mfma_f32_32x32x16_f16 v[50:65], v[140:143], v[144:147], v[50:65]
	v_mfma_f32_32x32x16_f16 v[2:17], v[140:143], v[148:151], v[2:17]
	s_waitcnt lgkmcnt(0)
	v_mfma_f32_32x32x16_f16 v[82:97], v[112:115], v[124:127], v[82:97]
	ds_read_b128 v[144:147], v104
	ds_read_b128 v[132:135], v102
	v_mfma_f32_32x32x16_f16 v[34:49], v[112:115], v[128:131], v[34:49]
	ds_read_b128 v[148:151], v104 offset:2048
	ds_read_b128 v[136:139], v102 offset:2048
	v_mfma_f32_32x32x16_f16 v[66:81], v[116:119], v[124:127], v[66:81]
	ds_read_b128 v[140:143], v102 offset:4096
	v_mfma_f32_32x32x16_f16 v[18:33], v[116:119], v[128:131], v[18:33]
	v_mfma_f32_32x32x16_f16 v[50:65], v[120:123], v[124:127], v[50:65]
	v_mfma_f32_32x32x16_f16 v[2:17], v[120:123], v[128:131], v[2:17]
	s_waitcnt lgkmcnt(0)
	s_barrier
	v_mfma_f32_32x32x16_f16 v[82:97], v[132:135], v[144:147], v[82:97]
	ds_read_b128 v[124:127], v103 offset:28672
	ds_read_b128 v[112:115], v101 offset:28672
	v_mfma_f32_32x32x16_f16 v[34:49], v[132:135], v[148:151], v[34:49]
	ds_read_b128 v[128:131], v103 offset:30720
	ds_read_b128 v[116:119], v101 offset:30720
	v_mfma_f32_32x32x16_f16 v[66:81], v[136:139], v[144:147], v[66:81]
	ds_read_b128 v[120:123], v101 offset:32768
	v_mfma_f32_32x32x16_f16 v[18:33], v[136:139], v[148:151], v[18:33]
	v_mfma_f32_32x32x16_f16 v[50:65], v[140:143], v[144:147], v[50:65]
	v_mfma_f32_32x32x16_f16 v[2:17], v[140:143], v[148:151], v[2:17]
	s_waitcnt lgkmcnt(0)
	v_mfma_f32_32x32x16_f16 v[82:97], v[112:115], v[124:127], v[82:97]
	ds_read_b128 v[144:147], v104 offset:28672
	ds_read_b128 v[132:135], v102 offset:28672
	v_mfma_f32_32x32x16_f16 v[34:49], v[112:115], v[128:131], v[34:49]
	ds_read_b128 v[148:151], v104 offset:30720
	ds_read_b128 v[136:139], v102 offset:30720
	v_mfma_f32_32x32x16_f16 v[66:81], v[116:119], v[124:127], v[66:81]
	ds_read_b128 v[140:143], v102 offset:32768
	v_mfma_f32_32x32x16_f16 v[18:33], v[116:119], v[128:131], v[18:33]
	v_mfma_f32_32x32x16_f16 v[50:65], v[120:123], v[124:127], v[50:65]
	v_mfma_f32_32x32x16_f16 v[2:17], v[120:123], v[128:131], v[2:17]
	s_waitcnt lgkmcnt(0)
	s_barrier
	v_mfma_f32_32x32x16_f16 v[82:97], v[132:135], v[144:147], v[82:97]
	ds_read_b128 v[124:127], v107
	ds_read_b128 v[112:115], v105
	v_mfma_f32_32x32x16_f16 v[34:49], v[132:135], v[148:151], v[34:49]
	ds_read_b128 v[128:131], v107 offset:2048
	ds_read_b128 v[116:119], v105 offset:2048
	v_mfma_f32_32x32x16_f16 v[66:81], v[136:139], v[144:147], v[66:81]
	ds_read_b128 v[120:123], v105 offset:4096
	v_mfma_f32_32x32x16_f16 v[18:33], v[136:139], v[148:151], v[18:33]
	v_mfma_f32_32x32x16_f16 v[50:65], v[140:143], v[144:147], v[50:65]
	v_mfma_f32_32x32x16_f16 v[2:17], v[140:143], v[148:151], v[2:17]
	s_waitcnt lgkmcnt(0)
	v_mfma_f32_32x32x16_f16 v[82:97], v[112:115], v[124:127], v[82:97]
	ds_read_b128 v[144:147], v108
	ds_read_b128 v[132:135], v106
	v_mfma_f32_32x32x16_f16 v[34:49], v[112:115], v[128:131], v[34:49]
	ds_read_b128 v[148:151], v108 offset:2048
	ds_read_b128 v[136:139], v106 offset:2048
	v_mfma_f32_32x32x16_f16 v[66:81], v[116:119], v[124:127], v[66:81]
	ds_read_b128 v[140:143], v106 offset:4096
	v_mfma_f32_32x32x16_f16 v[18:33], v[116:119], v[128:131], v[18:33]
	v_mfma_f32_32x32x16_f16 v[50:65], v[120:123], v[124:127], v[50:65]
	v_mfma_f32_32x32x16_f16 v[2:17], v[120:123], v[128:131], v[2:17]
	s_waitcnt lgkmcnt(0)
	s_barrier
	v_mfma_f32_32x32x16_f16 v[82:97], v[132:135], v[144:147], v[82:97]
	ds_read_b128 v[124:127], v107 offset:28672
	ds_read_b128 v[112:115], v105 offset:28672
	v_mfma_f32_32x32x16_f16 v[34:49], v[132:135], v[148:151], v[34:49]
	ds_read_b128 v[128:131], v107 offset:30720
	ds_read_b128 v[116:119], v105 offset:30720
	v_mfma_f32_32x32x16_f16 v[66:81], v[136:139], v[144:147], v[66:81]
	ds_read_b128 v[120:123], v105 offset:32768
	v_mfma_f32_32x32x16_f16 v[18:33], v[136:139], v[148:151], v[18:33]
	v_mfma_f32_32x32x16_f16 v[50:65], v[140:143], v[144:147], v[50:65]
	v_mfma_f32_32x32x16_f16 v[2:17], v[140:143], v[148:151], v[2:17]
	s_waitcnt lgkmcnt(0)
	v_mfma_f32_32x32x16_f16 v[82:97], v[112:115], v[124:127], v[82:97]
	ds_read_b128 v[144:147], v108 offset:28672
	ds_read_b128 v[132:135], v106 offset:28672
	v_mfma_f32_32x32x16_f16 v[34:49], v[112:115], v[128:131], v[34:49]
	ds_read_b128 v[148:151], v108 offset:30720
	ds_read_b128 v[136:139], v106 offset:30720
	v_mfma_f32_32x32x16_f16 v[66:81], v[116:119], v[124:127], v[66:81]
	ds_read_b128 v[140:143], v106 offset:32768
	v_mfma_f32_32x32x16_f16 v[18:33], v[116:119], v[128:131], v[18:33]
	v_mfma_f32_32x32x16_f16 v[50:65], v[120:123], v[124:127], v[50:65]
	v_mfma_f32_32x32x16_f16 v[2:17], v[120:123], v[128:131], v[2:17]
	s_waitcnt lgkmcnt(0)
	s_barrier
	v_mfma_f32_32x32x16_f16 v[82:97], v[132:135], v[144:147], v[82:97]
	ds_read_b128 v[124:127], v154
	ds_read_b128 v[112:115], v152
	v_mfma_f32_32x32x16_f16 v[34:49], v[132:135], v[148:151], v[34:49]
	ds_read_b128 v[128:131], v154 offset:2048
	ds_read_b128 v[116:119], v152 offset:2048
	v_mfma_f32_32x32x16_f16 v[66:81], v[136:139], v[144:147], v[66:81]
	ds_read_b128 v[120:123], v152 offset:4096
	v_mfma_f32_32x32x16_f16 v[18:33], v[136:139], v[148:151], v[18:33]
	v_mfma_f32_32x32x16_f16 v[50:65], v[140:143], v[144:147], v[50:65]
	v_mfma_f32_32x32x16_f16 v[2:17], v[140:143], v[148:151], v[2:17]
	s_waitcnt lgkmcnt(0)
	v_mfma_f32_32x32x16_f16 v[82:97], v[112:115], v[124:127], v[82:97]
	ds_read_b128 v[144:147], v155
	ds_read_b128 v[132:135], v153
	v_mfma_f32_32x32x16_f16 v[34:49], v[112:115], v[128:131], v[34:49]
	ds_read_b128 v[148:151], v155 offset:2048
	ds_read_b128 v[136:139], v153 offset:2048
	v_mfma_f32_32x32x16_f16 v[66:81], v[116:119], v[124:127], v[66:81]
	ds_read_b128 v[140:143], v153 offset:4096
	v_mfma_f32_32x32x16_f16 v[18:33], v[116:119], v[128:131], v[18:33]
	v_mfma_f32_32x32x16_f16 v[50:65], v[120:123], v[124:127], v[50:65]
	v_mfma_f32_32x32x16_f16 v[2:17], v[120:123], v[128:131], v[2:17]
	s_waitcnt lgkmcnt(0)
	s_barrier
	v_mfma_f32_32x32x16_f16 v[82:97], v[132:135], v[144:147], v[82:97]
	ds_read_b128 v[124:127], v103
	ds_read_b128 v[112:115], v101
	v_mfma_f32_32x32x16_f16 v[34:49], v[132:135], v[148:151], v[34:49]
	ds_read_b128 v[128:131], v103 offset:2048
	ds_read_b128 v[116:119], v101 offset:2048
	v_mfma_f32_32x32x16_f16 v[66:81], v[136:139], v[144:147], v[66:81]
	ds_read_b128 v[120:123], v101 offset:4096
	v_mfma_f32_32x32x16_f16 v[18:33], v[136:139], v[148:151], v[18:33]
	v_mfma_f32_32x32x16_f16 v[50:65], v[140:143], v[144:147], v[50:65]
	v_mfma_f32_32x32x16_f16 v[2:17], v[140:143], v[148:151], v[2:17]
	s_waitcnt lgkmcnt(0)
	v_mfma_f32_32x32x16_f16 v[82:97], v[112:115], v[124:127], v[82:97]
	ds_read_b128 v[144:147], v104
	ds_read_b128 v[132:135], v102
	v_mfma_f32_32x32x16_f16 v[34:49], v[112:115], v[128:131], v[34:49]
	ds_read_b128 v[148:151], v104 offset:2048
	ds_read_b128 v[136:139], v102 offset:2048
	v_mfma_f32_32x32x16_f16 v[66:81], v[116:119], v[124:127], v[66:81]
	ds_read_b128 v[140:143], v102 offset:4096
	v_mfma_f32_32x32x16_f16 v[18:33], v[116:119], v[128:131], v[18:33]
	v_mfma_f32_32x32x16_f16 v[50:65], v[120:123], v[124:127], v[50:65]
	v_mfma_f32_32x32x16_f16 v[2:17], v[120:123], v[128:131], v[2:17]
	s_waitcnt lgkmcnt(0)
	s_barrier
	v_mfma_f32_32x32x16_f16 v[82:97], v[132:135], v[144:147], v[82:97]
	ds_read_b128 v[124:127], v103 offset:28672
	ds_read_b128 v[112:115], v101 offset:28672
	v_mfma_f32_32x32x16_f16 v[34:49], v[132:135], v[148:151], v[34:49]
	ds_read_b128 v[128:131], v103 offset:30720
	ds_read_b128 v[116:119], v101 offset:30720
	v_mfma_f32_32x32x16_f16 v[66:81], v[136:139], v[144:147], v[66:81]
	ds_read_b128 v[120:123], v101 offset:32768
	v_mfma_f32_32x32x16_f16 v[18:33], v[136:139], v[148:151], v[18:33]
	v_mfma_f32_32x32x16_f16 v[50:65], v[140:143], v[144:147], v[50:65]
	v_mfma_f32_32x32x16_f16 v[2:17], v[140:143], v[148:151], v[2:17]
	s_waitcnt lgkmcnt(0)
	v_mfma_f32_32x32x16_f16 v[82:97], v[112:115], v[124:127], v[82:97]
	ds_read_b128 v[144:147], v104 offset:28672
	ds_read_b128 v[132:135], v102 offset:28672
	v_mfma_f32_32x32x16_f16 v[34:49], v[112:115], v[128:131], v[34:49]
	ds_read_b128 v[148:151], v104 offset:30720
	ds_read_b128 v[136:139], v102 offset:30720
	v_mfma_f32_32x32x16_f16 v[66:81], v[116:119], v[124:127], v[66:81]
	ds_read_b128 v[140:143], v102 offset:32768
	v_mfma_f32_32x32x16_f16 v[18:33], v[116:119], v[128:131], v[18:33]
	v_mfma_f32_32x32x16_f16 v[50:65], v[120:123], v[124:127], v[50:65]
	v_mfma_f32_32x32x16_f16 v[2:17], v[120:123], v[128:131], v[2:17]
	s_waitcnt lgkmcnt(0)
	s_barrier
	v_mfma_f32_32x32x16_f16 v[82:97], v[132:135], v[144:147], v[82:97]
	ds_read_b128 v[124:127], v107
	ds_read_b128 v[112:115], v105
	v_mfma_f32_32x32x16_f16 v[34:49], v[132:135], v[148:151], v[34:49]
	ds_read_b128 v[128:131], v107 offset:2048
	ds_read_b128 v[116:119], v105 offset:2048
	v_mfma_f32_32x32x16_f16 v[66:81], v[136:139], v[144:147], v[66:81]
	ds_read_b128 v[120:123], v105 offset:4096
	v_mfma_f32_32x32x16_f16 v[18:33], v[136:139], v[148:151], v[18:33]
	v_mfma_f32_32x32x16_f16 v[50:65], v[140:143], v[144:147], v[50:65]
	v_mfma_f32_32x32x16_f16 v[2:17], v[140:143], v[148:151], v[2:17]
	s_waitcnt lgkmcnt(0)
	v_mfma_f32_32x32x16_f16 v[82:97], v[112:115], v[124:127], v[82:97]
	ds_read_b128 v[144:147], v108
	ds_read_b128 v[132:135], v106
	v_mfma_f32_32x32x16_f16 v[34:49], v[112:115], v[128:131], v[34:49]
	ds_read_b128 v[148:151], v108 offset:2048
	ds_read_b128 v[136:139], v106 offset:2048
	v_mfma_f32_32x32x16_f16 v[66:81], v[116:119], v[124:127], v[66:81]
	ds_read_b128 v[140:143], v106 offset:4096
	v_mfma_f32_32x32x16_f16 v[18:33], v[116:119], v[128:131], v[18:33]
	v_mfma_f32_32x32x16_f16 v[50:65], v[120:123], v[124:127], v[50:65]
	v_mfma_f32_32x32x16_f16 v[2:17], v[120:123], v[128:131], v[2:17]
	s_waitcnt lgkmcnt(0)
	s_barrier
	v_mfma_f32_32x32x16_f16 v[82:97], v[132:135], v[144:147], v[82:97]
	ds_read_b128 v[124:127], v107 offset:28672
	ds_read_b128 v[112:115], v105 offset:28672
	v_mfma_f32_32x32x16_f16 v[34:49], v[132:135], v[148:151], v[34:49]
	ds_read_b128 v[128:131], v107 offset:30720
	ds_read_b128 v[116:119], v105 offset:30720
	v_mfma_f32_32x32x16_f16 v[66:81], v[136:139], v[144:147], v[66:81]
	ds_read_b128 v[120:123], v105 offset:32768
	v_mfma_f32_32x32x16_f16 v[18:33], v[136:139], v[148:151], v[18:33]
	v_mfma_f32_32x32x16_f16 v[50:65], v[140:143], v[144:147], v[50:65]
	v_mfma_f32_32x32x16_f16 v[2:17], v[140:143], v[148:151], v[2:17]
	s_waitcnt lgkmcnt(0)
	v_mfma_f32_32x32x16_f16 v[82:97], v[112:115], v[124:127], v[82:97]
	ds_read_b128 v[144:147], v108 offset:28672
	ds_read_b128 v[132:135], v106 offset:28672
	v_mfma_f32_32x32x16_f16 v[34:49], v[112:115], v[128:131], v[34:49]
	ds_read_b128 v[148:151], v108 offset:30720
	ds_read_b128 v[136:139], v106 offset:30720
	v_mfma_f32_32x32x16_f16 v[66:81], v[116:119], v[124:127], v[66:81]
	ds_read_b128 v[140:143], v106 offset:32768
	v_mfma_f32_32x32x16_f16 v[18:33], v[116:119], v[128:131], v[18:33]
	v_mfma_f32_32x32x16_f16 v[50:65], v[120:123], v[124:127], v[50:65]
	v_mfma_f32_32x32x16_f16 v[2:17], v[120:123], v[128:131], v[2:17]
	s_waitcnt lgkmcnt(0)
	s_barrier
	v_mfma_f32_32x32x16_f16 v[82:97], v[132:135], v[144:147], v[82:97]
	ds_read_b128 v[124:127], v154
	ds_read_b128 v[112:115], v152
	v_mfma_f32_32x32x16_f16 v[34:49], v[132:135], v[148:151], v[34:49]
	ds_read_b128 v[128:131], v154 offset:2048
	ds_read_b128 v[116:119], v152 offset:2048
	v_mfma_f32_32x32x16_f16 v[66:81], v[136:139], v[144:147], v[66:81]
	ds_read_b128 v[120:123], v152 offset:4096
	v_mfma_f32_32x32x16_f16 v[18:33], v[136:139], v[148:151], v[18:33]
	v_mfma_f32_32x32x16_f16 v[50:65], v[140:143], v[144:147], v[50:65]
	v_mfma_f32_32x32x16_f16 v[2:17], v[140:143], v[148:151], v[2:17]
	s_waitcnt lgkmcnt(0)
	v_mfma_f32_32x32x16_f16 v[82:97], v[112:115], v[124:127], v[82:97]
	ds_read_b128 v[144:147], v155
	ds_read_b128 v[132:135], v153
	v_mfma_f32_32x32x16_f16 v[34:49], v[112:115], v[128:131], v[34:49]
	ds_read_b128 v[148:151], v155 offset:2048
	ds_read_b128 v[136:139], v153 offset:2048
	v_mfma_f32_32x32x16_f16 v[66:81], v[116:119], v[124:127], v[66:81]
	ds_read_b128 v[140:143], v153 offset:4096
	v_mfma_f32_32x32x16_f16 v[18:33], v[116:119], v[128:131], v[18:33]
	v_mfma_f32_32x32x16_f16 v[50:65], v[120:123], v[124:127], v[50:65]
	v_mfma_f32_32x32x16_f16 v[2:17], v[120:123], v[128:131], v[2:17]
	s_waitcnt lgkmcnt(0)
	s_barrier
	v_mfma_f32_32x32x16_f16 v[82:97], v[132:135], v[144:147], v[82:97]
	ds_read_b128 v[124:127], v103
	ds_read_b128 v[112:115], v101
	v_mfma_f32_32x32x16_f16 v[34:49], v[132:135], v[148:151], v[34:49]
	ds_read_b128 v[128:131], v103 offset:2048
	ds_read_b128 v[116:119], v101 offset:2048
	v_mfma_f32_32x32x16_f16 v[66:81], v[136:139], v[144:147], v[66:81]
	ds_read_b128 v[120:123], v101 offset:4096
	v_mfma_f32_32x32x16_f16 v[18:33], v[136:139], v[148:151], v[18:33]
	v_mfma_f32_32x32x16_f16 v[50:65], v[140:143], v[144:147], v[50:65]
	v_mfma_f32_32x32x16_f16 v[2:17], v[140:143], v[148:151], v[2:17]
	s_waitcnt lgkmcnt(0)
	v_mfma_f32_32x32x16_f16 v[82:97], v[112:115], v[124:127], v[82:97]
	ds_read_b128 v[144:147], v104
	ds_read_b128 v[132:135], v102
	v_mfma_f32_32x32x16_f16 v[34:49], v[112:115], v[128:131], v[34:49]
	ds_read_b128 v[148:151], v104 offset:2048
	ds_read_b128 v[136:139], v102 offset:2048
	v_mfma_f32_32x32x16_f16 v[66:81], v[116:119], v[124:127], v[66:81]
	ds_read_b128 v[140:143], v102 offset:4096
	v_mfma_f32_32x32x16_f16 v[18:33], v[116:119], v[128:131], v[18:33]
	v_mfma_f32_32x32x16_f16 v[50:65], v[120:123], v[124:127], v[50:65]
	v_mfma_f32_32x32x16_f16 v[2:17], v[120:123], v[128:131], v[2:17]
	s_waitcnt lgkmcnt(0)
	s_barrier
	v_mfma_f32_32x32x16_f16 v[82:97], v[132:135], v[144:147], v[82:97]
	ds_read_b128 v[124:127], v103 offset:28672
	ds_read_b128 v[112:115], v101 offset:28672
	v_mfma_f32_32x32x16_f16 v[34:49], v[132:135], v[148:151], v[34:49]
	ds_read_b128 v[128:131], v103 offset:30720
	ds_read_b128 v[116:119], v101 offset:30720
	v_mfma_f32_32x32x16_f16 v[66:81], v[136:139], v[144:147], v[66:81]
	ds_read_b128 v[120:123], v101 offset:32768
	v_mfma_f32_32x32x16_f16 v[18:33], v[136:139], v[148:151], v[18:33]
	v_mfma_f32_32x32x16_f16 v[50:65], v[140:143], v[144:147], v[50:65]
	v_mfma_f32_32x32x16_f16 v[2:17], v[140:143], v[148:151], v[2:17]
	s_waitcnt lgkmcnt(0)
	v_mfma_f32_32x32x16_f16 v[82:97], v[112:115], v[124:127], v[82:97]
	ds_read_b128 v[144:147], v104 offset:28672
	ds_read_b128 v[132:135], v102 offset:28672
	v_mfma_f32_32x32x16_f16 v[34:49], v[112:115], v[128:131], v[34:49]
	ds_read_b128 v[148:151], v104 offset:30720
	ds_read_b128 v[136:139], v102 offset:30720
	v_mfma_f32_32x32x16_f16 v[66:81], v[116:119], v[124:127], v[66:81]
	ds_read_b128 v[140:143], v102 offset:32768
	v_mfma_f32_32x32x16_f16 v[18:33], v[116:119], v[128:131], v[18:33]
	v_mfma_f32_32x32x16_f16 v[50:65], v[120:123], v[124:127], v[50:65]
	v_mfma_f32_32x32x16_f16 v[2:17], v[120:123], v[128:131], v[2:17]
	s_waitcnt lgkmcnt(0)
	s_barrier
	v_mfma_f32_32x32x16_f16 v[82:97], v[132:135], v[144:147], v[82:97]
	ds_read_b128 v[124:127], v107
	ds_read_b128 v[112:115], v105
	v_mfma_f32_32x32x16_f16 v[34:49], v[132:135], v[148:151], v[34:49]
	ds_read_b128 v[128:131], v107 offset:2048
	ds_read_b128 v[116:119], v105 offset:2048
	v_mfma_f32_32x32x16_f16 v[66:81], v[136:139], v[144:147], v[66:81]
	ds_read_b128 v[120:123], v105 offset:4096
	v_mfma_f32_32x32x16_f16 v[18:33], v[136:139], v[148:151], v[18:33]
	v_mfma_f32_32x32x16_f16 v[50:65], v[140:143], v[144:147], v[50:65]
	v_mfma_f32_32x32x16_f16 v[2:17], v[140:143], v[148:151], v[2:17]
	s_waitcnt lgkmcnt(0)
	v_mfma_f32_32x32x16_f16 v[82:97], v[112:115], v[124:127], v[82:97]
	ds_read_b128 v[144:147], v108
	ds_read_b128 v[132:135], v106
	v_mfma_f32_32x32x16_f16 v[34:49], v[112:115], v[128:131], v[34:49]
	ds_read_b128 v[148:151], v108 offset:2048
	ds_read_b128 v[136:139], v106 offset:2048
	v_mfma_f32_32x32x16_f16 v[66:81], v[116:119], v[124:127], v[66:81]
	ds_read_b128 v[140:143], v106 offset:4096
	v_mfma_f32_32x32x16_f16 v[18:33], v[116:119], v[128:131], v[18:33]
	v_mfma_f32_32x32x16_f16 v[50:65], v[120:123], v[124:127], v[50:65]
	v_mfma_f32_32x32x16_f16 v[2:17], v[120:123], v[128:131], v[2:17]
	s_waitcnt lgkmcnt(0)
	s_barrier
	v_mfma_f32_32x32x16_f16 v[82:97], v[132:135], v[144:147], v[82:97]
	ds_read_b128 v[124:127], v107 offset:28672
	ds_read_b128 v[112:115], v105 offset:28672
	v_mfma_f32_32x32x16_f16 v[34:49], v[132:135], v[148:151], v[34:49]
	ds_read_b128 v[128:131], v107 offset:30720
	ds_read_b128 v[116:119], v105 offset:30720
	v_mfma_f32_32x32x16_f16 v[66:81], v[136:139], v[144:147], v[66:81]
	ds_read_b128 v[120:123], v105 offset:32768
	v_mfma_f32_32x32x16_f16 v[18:33], v[136:139], v[148:151], v[18:33]
	v_mfma_f32_32x32x16_f16 v[50:65], v[140:143], v[144:147], v[50:65]
	v_mfma_f32_32x32x16_f16 v[2:17], v[140:143], v[148:151], v[2:17]
	s_waitcnt lgkmcnt(0)
	v_mfma_f32_32x32x16_f16 v[82:97], v[112:115], v[124:127], v[82:97]
	ds_read_b128 v[144:147], v108 offset:28672
	ds_read_b128 v[132:135], v106 offset:28672
	v_mfma_f32_32x32x16_f16 v[34:49], v[112:115], v[128:131], v[34:49]
	ds_read_b128 v[148:151], v108 offset:30720
	ds_read_b128 v[136:139], v106 offset:30720
	v_mfma_f32_32x32x16_f16 v[66:81], v[116:119], v[124:127], v[66:81]
	ds_read_b128 v[140:143], v106 offset:32768
	v_mfma_f32_32x32x16_f16 v[18:33], v[116:119], v[128:131], v[18:33]
	v_mfma_f32_32x32x16_f16 v[50:65], v[120:123], v[124:127], v[50:65]
	v_mfma_f32_32x32x16_f16 v[2:17], v[120:123], v[128:131], v[2:17]
	s_waitcnt lgkmcnt(0)
	v_mfma_f32_32x32x16_f16 v[82:97], v[132:135], v[144:147], v[82:97]
	v_mfma_f32_32x32x16_f16 v[34:49], v[132:135], v[148:151], v[34:49]
	v_mfma_f32_32x32x16_f16 v[66:81], v[136:139], v[144:147], v[66:81]
	v_mfma_f32_32x32x16_f16 v[18:33], v[136:139], v[148:151], v[18:33]
	v_mfma_f32_32x32x16_f16 v[50:65], v[140:143], v[144:147], v[50:65]
	v_mfma_f32_32x32x16_f16 v[2:17], v[140:143], v[148:151], v[2:17]
	s_branch .LBB1_35

.LBB2_4:
	s_setprio 2
	s_load_dwordx4 s[4:7], s[0:1], 0x0
	s_add_i32 s13, s13, -4
	v_lshrrev_b32_e32 v1, 3, v1
	v_and_b32_e32 v30, 7, v0
	s_mul_i32 s10, s8, 0x600
	s_mul_i32 s11, s9, 0x600
	s_waitcnt lgkmcnt(0)
	s_add_u32 s4, s4, s10
	s_addc_u32 s5, s5, 0
	s_add_u32 s6, s6, s11
	s_addc_u32 s7, s7, 0
	s_cmp_eq_u32 s13, 1
	s_cselect_b32 s14, s6, s4
	s_cselect_b32 s15, s7, s5
	s_cselect_b32 s16, 0xffffa000, 0
	s_mul_i32 s17, s13, 0x2a000
	s_add_u32 s4, s4, s17
	s_addc_u32 s5, s5, 0
	s_ashr_i32 s17, s16, 31
	s_add_u32 s14, s14, s16
	s_addc_u32 s15, s15, s17
	v_and_b32_e32 v31, 63, v0
	v_lshrrev_b32_e32 v32, 4, v31
	v_xor_b32_e32 v32, v32, v30
	v_lshlrev_b32_e32 v32, 4, v32
	v_mul_u32_u24_e32 v2, 0x600, v1
	v_add_u32_e32 v2, v2, v32
	v_xor_b32_e32 v3, 64, v2
	s_add_u32 s20, s4, 0x0
	s_addc_u32 s21, s5, 0
	s_add_u32 s22, s4, 0x3000
	s_addc_u32 s23, s5, 0
	s_add_u32 s24, s14, 0x6000
	s_addc_u32 s25, s15, 0
	s_add_u32 s26, s14, 0x9000
	s_addc_u32 s27, s15, 0
	s_add_u32 s28, s14, 0xc000
	s_addc_u32 s29, s15, 0
	s_add_u32 s30, s14, 0xf000
	s_addc_u32 s31, s15, 0
	s_add_u32 s32, s14, 0x12000
	s_addc_u32 s33, s15, 0
	s_add_u32 s34, s14, 0x15000
	s_addc_u32 s35, s15, 0
	s_add_u32 s36, s14, 0x18000
	s_addc_u32 s37, s15, 0
	s_add_u32 s38, s14, 0x1b000
	s_addc_u32 s39, s15, 0
	s_add_u32 s40, s14, 0x1e000
	s_addc_u32 s41, s15, 0
	s_add_u32 s42, s14, 0x21000
	s_addc_u32 s43, s15, 0
	s_add_u32 s44, s14, 0x24000
	s_addc_u32 s45, s15, 0
	s_add_u32 s46, s14, 0x27000
	s_addc_u32 s47, s15, 0
	s_mul_i32 s18, s13, 0x3800
	s_add_i32 m0, s18, 2048
	s_nop 0
	global_load_lds_dwordx4 v2, s[20:21]
	s_add_i32 m0, s18, 3072
	s_nop 0
	global_load_lds_dwordx4 v3, s[22:23]
	s_add_i32 m0, s18, 4096
	s_nop 0
	global_load_lds_dwordx4 v2, s[24:25]
	s_add_i32 m0, s18, 5120
	s_nop 0
	global_load_lds_dwordx4 v3, s[26:27]
	s_add_i32 m0, s18, 6144
	s_nop 0
	global_load_lds_dwordx4 v2, s[28:29]
	s_add_i32 m0, s18, 7168
	s_nop 0
	global_load_lds_dwordx4 v3, s[30:31]
	s_add_i32 m0, s18, 8192
	s_nop 0
	global_load_lds_dwordx4 v2, s[32:33]
	s_add_i32 m0, s18, 9216
	s_nop 0
	global_load_lds_dwordx4 v3, s[34:35]
	s_add_i32 m0, s18, 10240
	s_nop 0
	global_load_lds_dwordx4 v2, s[36:37]
	s_add_i32 m0, s18, 11264
	s_nop 0
	global_load_lds_dwordx4 v3, s[38:39]
	s_add_i32 m0, s18, 12288
	s_nop 0
	global_load_lds_dwordx4 v2, s[40:41]
	s_add_i32 m0, s18, 13312
	s_nop 0
	global_load_lds_dwordx4 v3, s[42:43]
	s_add_i32 m0, s18, 14336
	s_nop 0
	global_load_lds_dwordx4 v2, s[44:45]
	s_add_i32 m0, s18, 15360
	s_nop 0
	global_load_lds_dwordx4 v3, s[46:47]
	s_add_i32 m0, s18, 30592
	s_nop 0
	global_load_lds_dwordx4 v2, s[20:21] offset:128
	s_add_i32 m0, s18, 31616
	s_nop 0
	global_load_lds_dwordx4 v3, s[22:23] offset:128
	s_add_i32 m0, s18, 32640
	s_nop 0
	global_load_lds_dwordx4 v2, s[24:25] offset:128
	s_add_i32 m0, s18, 33664
	s_nop 0
	global_load_lds_dwordx4 v3, s[26:27] offset:128
	s_add_i32 m0, s18, 34688
	s_nop 0
	global_load_lds_dwordx4 v2, s[28:29] offset:128
	s_add_i32 m0, s18, 35712
	s_nop 0
	global_load_lds_dwordx4 v3, s[30:31] offset:128
	s_add_i32 m0, s18, 36736
	s_nop 0
	global_load_lds_dwordx4 v2, s[32:33] offset:128
	s_add_i32 m0, s18, 37760
	s_nop 0
	global_load_lds_dwordx4 v3, s[34:35] offset:128
	s_add_i32 m0, s18, 38784
	s_nop 0
	global_load_lds_dwordx4 v2, s[36:37] offset:128
	s_add_i32 m0, s18, 39808
	s_nop 0
	global_load_lds_dwordx4 v3, s[38:39] offset:128
	s_add_i32 m0, s18, 40832
	s_nop 0
	global_load_lds_dwordx4 v2, s[40:41] offset:128
	s_add_i32 m0, s18, 41856
	s_nop 0
	global_load_lds_dwordx4 v3, s[42:43] offset:128
	s_add_i32 m0, s18, 42880
	s_nop 0
	global_load_lds_dwordx4 v2, s[44:45] offset:128
	s_add_i32 m0, s18, 43904
	s_nop 0
	global_load_lds_dwordx4 v3, s[46:47] offset:128
	s_add_i32 m0, s18, 59136
	s_nop 0
	global_load_lds_dwordx4 v2, s[20:21] offset:256
	s_add_i32 m0, s18, 60160
	s_nop 0
	global_load_lds_dwordx4 v3, s[22:23] offset:256
	s_add_i32 m0, s18, 61184
	s_nop 0
	global_load_lds_dwordx4 v2, s[24:25] offset:256
	s_add_i32 m0, s18, 62208
	s_nop 0
	global_load_lds_dwordx4 v3, s[26:27] offset:256
	s_add_i32 m0, s18, 63232
	s_nop 0
	global_load_lds_dwordx4 v2, s[28:29] offset:256
	s_add_i32 m0, s18, 64256
	s_nop 0
	global_load_lds_dwordx4 v3, s[30:31] offset:256
	s_add_i32 m0, s18, 65280
	s_nop 0
	global_load_lds_dwordx4 v2, s[32:33] offset:256
	s_add_i32 m0, s18, 66304
	s_nop 0
	global_load_lds_dwordx4 v3, s[34:35] offset:256
	s_add_i32 m0, s18, 67328
	s_nop 0
	global_load_lds_dwordx4 v2, s[36:37] offset:256
	s_add_i32 m0, s18, 68352
	s_nop 0
	global_load_lds_dwordx4 v3, s[38:39] offset:256
	s_add_i32 m0, s18, 69376
	s_nop 0
	global_load_lds_dwordx4 v2, s[40:41] offset:256
	s_add_i32 m0, s18, 70400
	s_nop 0
	global_load_lds_dwordx4 v3, s[42:43] offset:256
	s_add_i32 m0, s18, 71424
	s_nop 0
	global_load_lds_dwordx4 v2, s[44:45] offset:256
	s_add_i32 m0, s18, 72448
	s_nop 0
	global_load_lds_dwordx4 v3, s[46:47] offset:256
	s_add_i32 m0, s18, 87680
	s_nop 0
	global_load_lds_dwordx4 v2, s[20:21] offset:384
	s_add_i32 m0, s18, 88704
	s_nop 0
	global_load_lds_dwordx4 v3, s[22:23] offset:384
	s_add_i32 m0, s18, 89728
	s_nop 0
	global_load_lds_dwordx4 v2, s[24:25] offset:384
	s_add_i32 m0, s18, 90752
	s_nop 0
	global_load_lds_dwordx4 v3, s[26:27] offset:384
	s_add_i32 m0, s18, 91776
	s_nop 0
	global_load_lds_dwordx4 v2, s[28:29] offset:384
	s_add_i32 m0, s18, 92800
	s_nop 0
	global_load_lds_dwordx4 v3, s[30:31] offset:384
	s_add_i32 m0, s18, 93824
	s_nop 0
	global_load_lds_dwordx4 v2, s[32:33] offset:384
	s_add_i32 m0, s18, 94848
	s_nop 0
	global_load_lds_dwordx4 v3, s[34:35] offset:384
	s_add_i32 m0, s18, 95872
	s_nop 0
	global_load_lds_dwordx4 v2, s[36:37] offset:384
	s_add_i32 m0, s18, 96896
	s_nop 0
	global_load_lds_dwordx4 v3, s[38:39] offset:384
	s_add_i32 m0, s18, 97920
	s_nop 0
	global_load_lds_dwordx4 v2, s[40:41] offset:384
	s_add_i32 m0, s18, 98944
	s_nop 0
	global_load_lds_dwordx4 v3, s[42:43] offset:384
	s_add_i32 m0, s18, 99968
	s_nop 0
	global_load_lds_dwordx4 v2, s[44:45] offset:384
	s_add_i32 m0, s18, 100992
	s_nop 0
	global_load_lds_dwordx4 v3, s[46:47] offset:384
	s_waitcnt vmcnt(42)
	s_barrier
	s_add_i32 m0, s18, 116224
	s_nop 0
	global_load_lds_dwordx4 v2, s[20:21] offset:512
	s_add_i32 m0, s18, 117248
	s_nop 0
	global_load_lds_dwordx4 v3, s[22:23] offset:512
	s_add_i32 m0, s18, 118272
	s_nop 0
	global_load_lds_dwordx4 v2, s[24:25] offset:512
	s_add_i32 m0, s18, 119296
	s_nop 0
	global_load_lds_dwordx4 v3, s[26:27] offset:512
	s_add_i32 m0, s18, 120320
	s_nop 0
	global_load_lds_dwordx4 v2, s[28:29] offset:512
	s_add_i32 m0, s18, 121344
	s_nop 0
	global_load_lds_dwordx4 v3, s[30:31] offset:512
	s_add_i32 m0, s18, 122368
	s_nop 0
	global_load_lds_dwordx4 v2, s[32:33] offset:512
	s_add_i32 m0, s18, 123392
	s_nop 0
	global_load_lds_dwordx4 v3, s[34:35] offset:512
	s_add_i32 m0, s18, 124416
	s_nop 0
	global_load_lds_dwordx4 v2, s[36:37] offset:512
	s_add_i32 m0, s18, 125440
	s_nop 0
	global_load_lds_dwordx4 v3, s[38:39] offset:512
	s_add_i32 m0, s18, 126464
	s_nop 0
	global_load_lds_dwordx4 v2, s[40:41] offset:512
	s_add_i32 m0, s18, 127488
	s_nop 0
	global_load_lds_dwordx4 v3, s[42:43] offset:512
	s_add_i32 m0, s18, 128512
	s_nop 0
	global_load_lds_dwordx4 v2, s[44:45] offset:512
	s_add_i32 m0, s18, 129536
	s_nop 0
	global_load_lds_dwordx4 v3, s[46:47] offset:512
	s_waitcnt vmcnt(42)
	s_barrier
	s_add_i32 m0, s18, 1408
	s_nop 0
	global_load_lds_dwordx4 v2, s[20:21] offset:640
	s_add_i32 m0, s18, 2432
	s_nop 0
	global_load_lds_dwordx4 v3, s[22:23] offset:640
	s_add_i32 m0, s18, 3456
	s_nop 0
	global_load_lds_dwordx4 v2, s[24:25] offset:640
	s_add_i32 m0, s18, 4480
	s_nop 0
	global_load_lds_dwordx4 v3, s[26:27] offset:640
	s_add_i32 m0, s18, 5504
	s_nop 0
	global_load_lds_dwordx4 v2, s[28:29] offset:640
	s_add_i32 m0, s18, 6528
	s_nop 0
	global_load_lds_dwordx4 v3, s[30:31] offset:640
	s_add_i32 m0, s18, 7552
	s_nop 0
	global_load_lds_dwordx4 v2, s[32:33] offset:640
	s_add_i32 m0, s18, 8576
	s_nop 0
	global_load_lds_dwordx4 v3, s[34:35] offset:640
	s_add_i32 m0, s18, 9600
	s_nop 0
	global_load_lds_dwordx4 v2, s[36:37] offset:640
	s_add_i32 m0, s18, 10624
	s_nop 0
	global_load_lds_dwordx4 v3, s[38:39] offset:640
	s_add_i32 m0, s18, 11648
	s_nop 0
	global_load_lds_dwordx4 v2, s[40:41] offset:640
	s_add_i32 m0, s18, 12672
	s_nop 0
	global_load_lds_dwordx4 v3, s[42:43] offset:640
	s_add_i32 m0, s18, 13696
	s_nop 0
	global_load_lds_dwordx4 v2, s[44:45] offset:640
	s_add_i32 m0, s18, 14720
	s_nop 0
	global_load_lds_dwordx4 v3, s[46:47] offset:640
	s_waitcnt vmcnt(42)
	s_barrier
	s_add_i32 m0, s18, 29952
	s_nop 0
	global_load_lds_dwordx4 v2, s[20:21] offset:768
	s_add_i32 m0, s18, 30976
	s_nop 0
	global_load_lds_dwordx4 v3, s[22:23] offset:768
	s_add_i32 m0, s18, 32000
	s_nop 0
	global_load_lds_dwordx4 v2, s[24:25] offset:768
	s_add_i32 m0, s18, 33024
	s_nop 0
	global_load_lds_dwordx4 v3, s[26:27] offset:768
	s_add_i32 m0, s18, 34048
	s_nop 0
	global_load_lds_dwordx4 v2, s[28:29] offset:768
	s_add_i32 m0, s18, 35072
	s_nop 0
	global_load_lds_dwordx4 v3, s[30:31] offset:768
	s_add_i32 m0, s18, 36096
	s_nop 0
	global_load_lds_dwordx4 v2, s[32:33] offset:768
	s_add_i32 m0, s18, 37120
	s_nop 0
	global_load_lds_dwordx4 v3, s[34:35] offset:768
	s_add_i32 m0, s18, 38144
	s_nop 0
	global_load_lds_dwordx4 v2, s[36:37] offset:768
	s_add_i32 m0, s18, 39168
	s_nop 0
	global_load_lds_dwordx4 v3, s[38:39] offset:768
	s_add_i32 m0, s18, 40192
	s_nop 0
	global_load_lds_dwordx4 v2, s[40:41] offset:768
	s_add_i32 m0, s18, 41216
	s_nop 0
	global_load_lds_dwordx4 v3, s[42:43] offset:768
	s_add_i32 m0, s18, 42240
	s_nop 0
	global_load_lds_dwordx4 v2, s[44:45] offset:768
	s_add_i32 m0, s18, 43264
	s_nop 0
	global_load_lds_dwordx4 v3, s[46:47] offset:768
	s_waitcnt vmcnt(42)
	s_barrier
	s_add_i32 m0, s18, 58496
	s_nop 0
	global_load_lds_dwordx4 v2, s[20:21] offset:896
	s_add_i32 m0, s18, 59520
	s_nop 0
	global_load_lds_dwordx4 v3, s[22:23] offset:896
	s_add_i32 m0, s18, 60544
	s_nop 0
	global_load_lds_dwordx4 v2, s[24:25] offset:896
	s_add_i32 m0, s18, 61568
	s_nop 0
	global_load_lds_dwordx4 v3, s[26:27] offset:896
	s_add_i32 m0, s18, 62592
	s_nop 0
	global_load_lds_dwordx4 v2, s[28:29] offset:896
	s_add_i32 m0, s18, 63616
	s_nop 0
	global_load_lds_dwordx4 v3, s[30:31] offset:896
	s_add_i32 m0, s18, 64640
	s_nop 0
	global_load_lds_dwordx4 v2, s[32:33] offset:896
	s_add_i32 m0, s18, 65664
	s_nop 0
	global_load_lds_dwordx4 v3, s[34:35] offset:896
	s_add_i32 m0, s18, 66688
	s_nop 0
	global_load_lds_dwordx4 v2, s[36:37] offset:896
	s_add_i32 m0, s18, 67712
	s_nop 0
	global_load_lds_dwordx4 v3, s[38:39] offset:896
	s_add_i32 m0, s18, 68736
	s_nop 0
	global_load_lds_dwordx4 v2, s[40:41] offset:896
	s_add_i32 m0, s18, 69760
	s_nop 0
	global_load_lds_dwordx4 v3, s[42:43] offset:896
	s_add_i32 m0, s18, 70784
	s_nop 0
	global_load_lds_dwordx4 v2, s[44:45] offset:896
	s_add_i32 m0, s18, 71808
	s_nop 0
	global_load_lds_dwordx4 v3, s[46:47] offset:896
	s_waitcnt vmcnt(42)
	s_barrier
	s_add_i32 m0, s18, 87040
	s_nop 0
	global_load_lds_dwordx4 v2, s[20:21] offset:1024
	s_add_i32 m0, s18, 88064
	s_nop 0
	global_load_lds_dwordx4 v3, s[22:23] offset:1024
	s_add_i32 m0, s18, 89088
	s_nop 0
	global_load_lds_dwordx4 v2, s[24:25] offset:1024
	s_add_i32 m0, s18, 90112
	s_nop 0
	global_load_lds_dwordx4 v3, s[26:27] offset:1024
	s_add_i32 m0, s18, 91136
	s_nop 0
	global_load_lds_dwordx4 v2, s[28:29] offset:1024
	s_add_i32 m0, s18, 92160
	s_nop 0
	global_load_lds_dwordx4 v3, s[30:31] offset:1024
	s_add_i32 m0, s18, 93184
	s_nop 0
	global_load_lds_dwordx4 v2, s[32:33] offset:1024
	s_add_i32 m0, s18, 94208
	s_nop 0
	global_load_lds_dwordx4 v3, s[34:35] offset:1024
	s_add_i32 m0, s18, 95232
	s_nop 0
	global_load_lds_dwordx4 v2, s[36:37] offset:1024
	s_add_i32 m0, s18, 96256
	s_nop 0
	global_load_lds_dwordx4 v3, s[38:39] offset:1024
	s_add_i32 m0, s18, 97280
	s_nop 0
	global_load_lds_dwordx4 v2, s[40:41] offset:1024
	s_add_i32 m0, s18, 98304
	s_nop 0
	global_load_lds_dwordx4 v3, s[42:43] offset:1024
	s_add_i32 m0, s18, 99328
	s_nop 0
	global_load_lds_dwordx4 v2, s[44:45] offset:1024
	s_add_i32 m0, s18, 100352
	s_nop 0
	global_load_lds_dwordx4 v3, s[46:47] offset:1024
	s_waitcnt vmcnt(42)
	s_barrier
	s_add_i32 m0, s18, 115584
	s_nop 0
	global_load_lds_dwordx4 v2, s[20:21] offset:1152
	s_add_i32 m0, s18, 116608
	s_nop 0
	global_load_lds_dwordx4 v3, s[22:23] offset:1152
	s_add_i32 m0, s18, 117632
	s_nop 0
	global_load_lds_dwordx4 v2, s[24:25] offset:1152
	s_add_i32 m0, s18, 118656
	s_nop 0
	global_load_lds_dwordx4 v3, s[26:27] offset:1152
	s_add_i32 m0, s18, 119680
	s_nop 0
	global_load_lds_dwordx4 v2, s[28:29] offset:1152
	s_add_i32 m0, s18, 120704
	s_nop 0
	global_load_lds_dwordx4 v3, s[30:31] offset:1152
	s_add_i32 m0, s18, 121728
	s_nop 0
	global_load_lds_dwordx4 v2, s[32:33] offset:1152
	s_add_i32 m0, s18, 122752
	s_nop 0
	global_load_lds_dwordx4 v3, s[34:35] offset:1152
	s_add_i32 m0, s18, 123776
	s_nop 0
	global_load_lds_dwordx4 v2, s[36:37] offset:1152
	s_add_i32 m0, s18, 124800
	s_nop 0
	global_load_lds_dwordx4 v3, s[38:39] offset:1152
	s_add_i32 m0, s18, 125824
	s_nop 0
	global_load_lds_dwordx4 v2, s[40:41] offset:1152
	s_add_i32 m0, s18, 126848
	s_nop 0
	global_load_lds_dwordx4 v3, s[42:43] offset:1152
	s_add_i32 m0, s18, 127872
	s_nop 0
	global_load_lds_dwordx4 v2, s[44:45] offset:1152
	s_add_i32 m0, s18, 128896
	s_nop 0
	global_load_lds_dwordx4 v3, s[46:47] offset:1152
	s_waitcnt vmcnt(42)
	s_barrier
	s_add_i32 m0, s18, 768
	s_nop 0
	global_load_lds_dwordx4 v2, s[20:21] offset:1280
	s_add_i32 m0, s18, 1792
	s_nop 0
	global_load_lds_dwordx4 v3, s[22:23] offset:1280
	s_add_i32 m0, s18, 2816
	s_nop 0
	global_load_lds_dwordx4 v2, s[24:25] offset:1280
	s_add_i32 m0, s18, 3840
	s_nop 0
	global_load_lds_dwordx4 v3, s[26:27] offset:1280
	s_add_i32 m0, s18, 4864
	s_nop 0
	global_load_lds_dwordx4 v2, s[28:29] offset:1280
	s_add_i32 m0, s18, 5888
	s_nop 0
	global_load_lds_dwordx4 v3, s[30:31] offset:1280
	s_add_i32 m0, s18, 6912
	s_nop 0
	global_load_lds_dwordx4 v2, s[32:33] offset:1280
	s_add_i32 m0, s18, 7936
	s_nop 0
	global_load_lds_dwordx4 v3, s[34:35] offset:1280
	s_add_i32 m0, s18, 8960
	s_nop 0
	global_load_lds_dwordx4 v2, s[36:37] offset:1280
	s_add_i32 m0, s18, 9984
	s_nop 0
	global_load_lds_dwordx4 v3, s[38:39] offset:1280
	s_add_i32 m0, s18, 11008
	s_nop 0
	global_load_lds_dwordx4 v2, s[40:41] offset:1280
	s_add_i32 m0, s18, 12032
	s_nop 0
	global_load_lds_dwordx4 v3, s[42:43] offset:1280
	s_add_i32 m0, s18, 13056
	s_nop 0
	global_load_lds_dwordx4 v2, s[44:45] offset:1280
	s_add_i32 m0, s18, 14080
	s_nop 0
	global_load_lds_dwordx4 v3, s[46:47] offset:1280
	s_waitcnt vmcnt(42)
	s_barrier
	s_add_i32 m0, s18, 29312
	s_nop 0
	global_load_lds_dwordx4 v2, s[20:21] offset:1408
	s_add_i32 m0, s18, 30336
	s_nop 0
	global_load_lds_dwordx4 v3, s[22:23] offset:1408
	s_add_i32 m0, s18, 31360
	s_nop 0
	global_load_lds_dwordx4 v2, s[24:25] offset:1408
	s_add_i32 m0, s18, 32384
	s_nop 0
	global_load_lds_dwordx4 v3, s[26:27] offset:1408
	s_add_i32 m0, s18, 33408
	s_nop 0
	global_load_lds_dwordx4 v2, s[28:29] offset:1408
	s_add_i32 m0, s18, 34432
	s_nop 0
	global_load_lds_dwordx4 v3, s[30:31] offset:1408
	s_add_i32 m0, s18, 35456
	s_nop 0
	global_load_lds_dwordx4 v2, s[32:33] offset:1408
	s_add_i32 m0, s18, 36480
	s_nop 0
	global_load_lds_dwordx4 v3, s[34:35] offset:1408
	s_add_i32 m0, s18, 37504
	s_nop 0
	global_load_lds_dwordx4 v2, s[36:37] offset:1408
	s_add_i32 m0, s18, 38528
	s_nop 0
	global_load_lds_dwordx4 v3, s[38:39] offset:1408
	s_add_i32 m0, s18, 39552
	s_nop 0
	global_load_lds_dwordx4 v2, s[40:41] offset:1408
	s_add_i32 m0, s18, 40576
	s_nop 0
	global_load_lds_dwordx4 v3, s[42:43] offset:1408
	s_add_i32 m0, s18, 41600
	s_nop 0
	global_load_lds_dwordx4 v2, s[44:45] offset:1408
	s_add_i32 m0, s18, 42624
	s_nop 0
	global_load_lds_dwordx4 v3, s[46:47] offset:1408
	s_waitcnt vmcnt(42)
	s_barrier
	s_waitcnt vmcnt(28)
	s_barrier
	s_waitcnt vmcnt(14)
	s_barrier
	s_waitcnt vmcnt(0)
	s_barrier
	s_endpgm
